# speedup vs baseline: 1.0153x; 1.0036x over previous
.LE_join25:
	v_mfma_f32_32x32x16_f16 v[16:31], a[192:195], v[164:167], v[16:31]
	ds_read_b128 v[164:167], v193 offset:41984
	v_fmac_f32_e32 v78, v228, v242
	v_fmac_f32_e32 v79, v228, v244
	v_mfma_f32_32x32x16_f16 v[0:15], a[196:199], v[168:171], v[0:15]
	ds_read_b128 v[168:171], v193 offset:43008
	v_fma_f32 v94, v231, v243, v246
	v_fma_f32 v95, v231, v245, v247
	v_mfma_f32_32x32x16_f16 v[16:31], a[196:199], v[172:175], v[16:31]
	ds_read_b128 v[172:175], v193 offset:44032
	global_load_lds_dwordx4 v192, s[44:45] offset:1024 sc1
	v_fmac_f32_e32 v94, v230, v242
	v_fmac_f32_e32 v95, v230, v244
	s_waitcnt lgkmcnt(4)
	v_mfma_f32_32x32x16_f16 v[0:15], a[200:203], v[176:179], v[0:15]
	ds_read_b128 v[176:179], v193 offset:45056
	s_and_b32 s64, s33, 1
	s_lshl_b32 s64, s64, 22
	s_add_u32 s64, s64, s50
	s_add_u32 s36, s6, s64
	s_addc_u32 s37, s7, 0
	s_lshl_b32 s64, s33, 3
	s_add_u32 s64, s64, s29
	s_lshl_b32 s64, s64, 5
	s_add_u32 s64, s64, s30
	s_lshl_b32 s64, s64, 2
	s_add_u32 s40, s8, s64
	s_addc_u32 s41, s9, 0
	s_lshl_b32 s64, s33, 11
	s_lshl_b32 s65, s29, 8
	s_add_u32 s64, s64, s65
	s_add_u32 s64, s64, 192
	s_lshl_b32 s64, s64, 3
	s_add_u32 s42, s12, s64
	s_addc_u32 s43, s13, 0
	v_mfma_f32_32x32x16_f16 v[16:31], a[200:203], v[180:183], v[16:31]
	ds_read_b128 v[180:183], v193 offset:46080
	v_mfma_f32_32x32x16_f16 v[0:15], a[204:207], v[184:187], v[0:15]
	ds_read_b128 v[184:187], v193 offset:47104
	v_mfma_f32_32x32x16_f16 v[16:31], a[204:207], v[188:191], v[16:31]
	ds_read_b128 v[188:191], v193 offset:48128
	global_load_lds_dwordx4 v192, s[44:45] offset:2048 sc1
	s_waitcnt lgkmcnt(4)
	v_mfma_f32_32x32x16_f16 v[0:15], a[208:211], v[160:163], v[0:15]
	ds_read_b128 v[160:163], v193 offset:49152
	v_mfma_f32_32x32x16_f16 v[16:31], a[208:211], v[164:167], v[16:31]
	ds_read_b128 v[164:167], v193 offset:50176
	v_mfma_f32_32x32x16_f16 v[0:15], a[212:215], v[168:171], v[0:15]
	ds_read_b128 v[168:171], v193 offset:51200
	v_mfma_f32_32x32x16_f16 v[16:31], a[212:215], v[172:175], v[16:31]
	ds_read_b128 v[172:175], v193 offset:52224
	global_load_lds_dwordx4 v192, s[44:45] offset:3072 sc1
	s_waitcnt lgkmcnt(4)
	v_mfma_f32_32x32x16_f16 v[0:15], a[216:219], v[176:179], v[0:15]
	ds_read_b128 v[176:179], v193 offset:53248
	v_mfma_f32_32x32x16_f16 v[16:31], a[216:219], v[180:183], v[16:31]
	ds_read_b128 v[180:183], v193 offset:54272
	v_mfma_f32_32x32x16_f16 v[0:15], a[220:223], v[184:187], v[0:15]
	ds_read_b128 v[184:187], v193 offset:55296
	v_mfma_f32_32x32x16_f16 v[16:31], a[220:223], v[188:191], v[16:31]
	ds_read_b128 v[188:191], v193 offset:56320
	s_add_u32 s44, s34, 0x9000
	s_addc_u32 s45, s35, 0
	s_mov_b32 m0, s55
	s_nop 0
	global_load_lds_dwordx4 v192, s[44:45] sc1
	s_waitcnt lgkmcnt(4)
	v_mfma_f32_32x32x16_f16 v[0:15], a[224:227], v[160:163], v[0:15]
	ds_read_b128 v[160:163], v193 offset:57344
	v_mfma_f32_32x32x16_f16 v[16:31], a[224:227], v[164:167], v[16:31]
	ds_read_b128 v[164:167], v193 offset:58368
	v_mfma_f32_32x32x16_f16 v[0:15], a[228:231], v[168:171], v[0:15]
	ds_read_b128 v[168:171], v193 offset:59392
	v_mfma_f32_32x32x16_f16 v[16:31], a[228:231], v[172:175], v[16:31]
	ds_read_b128 v[172:175], v193 offset:60416
	global_load_lds_dwordx4 v192, s[44:45] offset:1024 sc1
	s_waitcnt lgkmcnt(4)
	v_mfma_f32_32x32x16_f16 v[0:15], a[232:235], v[176:179], v[0:15]
	ds_read_b128 v[176:179], v193 offset:61440
	v_mfma_f32_32x32x16_f16 v[16:31], a[232:235], v[180:183], v[16:31]
	ds_read_b128 v[180:183], v193 offset:62464
	v_mfma_f32_32x32x16_f16 v[0:15], a[236:239], v[184:187], v[0:15]
	ds_read_b128 v[184:187], v193 offset:63488
	v_mfma_f32_32x32x16_f16 v[16:31], a[236:239], v[188:191], v[16:31]
	ds_read_b128 v[188:191], v193 offset:64512
	global_load_lds_dwordx4 v192, s[44:45] offset:2048 sc1
	s_waitcnt vmcnt(8)
	s_barrier
	s_waitcnt lgkmcnt(4)
	v_mfma_f32_32x32x16_f16 v[0:15], a[240:243], v[160:163], v[0:15]
	ds_read_b128 v[160:163], v192 offset:0
	v_mfma_f32_32x32x16_f16 v[16:31], a[240:243], v[164:167], v[16:31]
	ds_read_b128 v[164:167], v192 offset:1024
	v_mfma_f32_32x32x16_f16 v[0:15], a[244:247], v[168:171], v[0:15]
	ds_read_b128 v[168:171], v192 offset:2048
	v_mfma_f32_32x32x16_f16 v[16:31], a[244:247], v[172:175], v[16:31]
	ds_read_b128 v[172:175], v192 offset:3072
	global_load_lds_dwordx4 v192, s[44:45] offset:3072 sc1
	s_waitcnt lgkmcnt(4)
	v_mfma_f32_32x32x16_f16 v[0:15], a[248:251], v[176:179], v[0:15]
	ds_read_b128 v[176:179], v192 offset:4096
	v_mfma_f32_32x32x16_f16 v[16:31], a[248:251], v[180:183], v[16:31]
	ds_read_b128 v[180:183], v192 offset:5120
	v_mfma_f32_32x32x16_f16 v[0:15], a[252:255], v[184:187], v[0:15]
	ds_read_b128 v[184:187], v192 offset:6144
	v_mfma_f32_32x32x16_f16 v[16:31], a[252:255], v[188:191], v[16:31]
	ds_read_b128 v[188:191], v192 offset:7168
	s_add_u32 s44, s34, 0x10000
	s_addc_u32 s45, s35, 0
	s_mov_b32 m0, s56
	s_nop 0
	global_load_lds_dwordx4 v192, s[44:45] sc1
	s_nop 3
	global_load_dwordx2 v[228:229], v249, s[42:43] offset:0
	global_load_dwordx2 v[230:231], v249, s[42:43] offset:256
	s_waitcnt lgkmcnt(4)
	v_mfma_f32_32x32x16_f16 v[32:47], a[0:3], v[160:163], v[32:47]
	ds_read_b128 v[160:163], v192 offset:8192
	v_exp_f32_e32 v200, v0
	v_mfma_f32_32x32x16_f16 v[48:63], a[0:3], v[164:167], v[48:63]
	ds_read_b128 v[164:167], v192 offset:9216
	s_lshl_b32 s64, s71, 3
	s_add_u32 s64, s64, s29
	s_lshl_b32 s64, s64, 7
	s_add_u32 s38, s8, s64
	s_addc_u32 s39, s9, 0
	global_load_dword v251, v196, s[38:39] sc1
	v_exp_f32_e32 v201, v1
	v_add_f32_e32 v200, 1.0, v200
	v_mfma_f32_32x32x16_f16 v[32:47], a[4:7], v[168:171], v[32:47]
	ds_read_b128 v[168:171], v192 offset:10240
	v_exp_f32_e32 v202, v2
	v_add_f32_e32 v201, 1.0, v201
	v_mfma_f32_32x32x16_f16 v[48:63], a[4:7], v[172:175], v[48:63]
	ds_read_b128 v[172:175], v192 offset:11264
	global_load_lds_dwordx4 v192, s[44:45] offset:1024 sc1
	v_exp_f32_e32 v203, v3
	v_add_f32_e32 v202, 1.0, v202
	s_waitcnt lgkmcnt(4)
	v_mfma_f32_32x32x16_f16 v[32:47], a[8:11], v[176:179], v[32:47]
	ds_read_b128 v[176:179], v192 offset:12288
	v_exp_f32_e32 v204, v4
	v_add_f32_e32 v203, 1.0, v203
	v_mfma_f32_32x32x16_f16 v[48:63], a[8:11], v[180:183], v[48:63]
	ds_read_b128 v[180:183], v192 offset:13312
	v_exp_f32_e32 v205, v5
	v_add_f32_e32 v204, 1.0, v204
	v_mfma_f32_32x32x16_f16 v[32:47], a[12:15], v[184:187], v[32:47]
	ds_read_b128 v[184:187], v192 offset:14336
	v_exp_f32_e32 v206, v6
	v_add_f32_e32 v205, 1.0, v205
	v_mfma_f32_32x32x16_f16 v[48:63], a[12:15], v[188:191], v[48:63]
	ds_read_b128 v[188:191], v192 offset:15360
	global_load_lds_dwordx4 v192, s[44:45] offset:2048 sc1
	v_exp_f32_e32 v207, v7
	v_add_f32_e32 v206, 1.0, v206
	s_waitcnt lgkmcnt(4)
	v_mfma_f32_32x32x16_f16 v[32:47], a[16:19], v[160:163], v[32:47]
	ds_read_b128 v[160:163], v192 offset:16384
	v_exp_f32_e32 v208, v8
	v_add_f32_e32 v207, 1.0, v207
	v_mfma_f32_32x32x16_f16 v[48:63], a[16:19], v[164:167], v[48:63]
	ds_read_b128 v[164:167], v192 offset:17408
	v_exp_f32_e32 v209, v9
	v_add_f32_e32 v208, 1.0, v208
	v_mfma_f32_32x32x16_f16 v[32:47], a[20:23], v[168:171], v[32:47]
	ds_read_b128 v[168:171], v192 offset:18432
	v_exp_f32_e32 v210, v10
	v_add_f32_e32 v209, 1.0, v209
	v_mfma_f32_32x32x16_f16 v[48:63], a[20:23], v[172:175], v[48:63]
	ds_read_b128 v[172:175], v192 offset:19456
	global_load_lds_dwordx4 v192, s[44:45] offset:3072 sc1
	v_exp_f32_e32 v211, v11
	v_add_f32_e32 v210, 1.0, v210
	s_waitcnt lgkmcnt(4)
	v_mfma_f32_32x32x16_f16 v[32:47], a[24:27], v[176:179], v[32:47]
	ds_read_b128 v[176:179], v192 offset:20480
	v_exp_f32_e32 v212, v12
	v_add_f32_e32 v211, 1.0, v211
	v_mfma_f32_32x32x16_f16 v[48:63], a[24:27], v[180:183], v[48:63]
	ds_read_b128 v[180:183], v192 offset:21504
	v_exp_f32_e32 v213, v13
	v_add_f32_e32 v212, 1.0, v212
	v_mfma_f32_32x32x16_f16 v[32:47], a[28:31], v[184:187], v[32:47]
	ds_read_b128 v[184:187], v192 offset:22528
	v_exp_f32_e32 v214, v14
	v_add_f32_e32 v213, 1.0, v213
	v_mfma_f32_32x32x16_f16 v[48:63], a[28:31], v[188:191], v[48:63]
	ds_read_b128 v[188:191], v192 offset:23552
	s_add_u32 s44, s34, 0x11000
	s_addc_u32 s45, s35, 0
	s_mov_b32 m0, s57
	s_nop 0
	global_load_lds_dwordx4 v192, s[44:45] sc1
	v_exp_f32_e32 v215, v15
	v_add_f32_e32 v214, 1.0, v214
	s_waitcnt lgkmcnt(4)
	v_mfma_f32_32x32x16_f16 v[32:47], a[32:35], v[160:163], v[32:47]
	ds_read_b128 v[160:163], v192 offset:24576
	v_add_f32_e32 v215, 1.0, v215
	v_rcp_f32_e32 v200, v200
	v_mfma_f32_32x32x16_f16 v[48:63], a[32:35], v[164:167], v[48:63]
	ds_read_b128 v[164:167], v192 offset:25600
	v_rcp_f32_e32 v201, v201
	v_mfma_f32_32x32x16_f16 v[32:47], a[36:39], v[168:171], v[32:47]
	ds_read_b128 v[168:171], v192 offset:26624
	v_rcp_f32_e32 v202, v202
	v_mfma_f32_32x32x16_f16 v[48:63], a[36:39], v[172:175], v[48:63]
	ds_read_b128 v[172:175], v192 offset:27648
	global_load_lds_dwordx4 v192, s[44:45] offset:1024 sc1
	v_rcp_f32_e32 v203, v203
	s_waitcnt lgkmcnt(4)
	v_mfma_f32_32x32x16_f16 v[32:47], a[40:43], v[176:179], v[32:47]
	ds_read_b128 v[176:179], v192 offset:28672
	v_rcp_f32_e32 v204, v204
	v_mfma_f32_32x32x16_f16 v[48:63], a[40:43], v[180:183], v[48:63]
	ds_read_b128 v[180:183], v192 offset:29696
	v_rcp_f32_e32 v205, v205
	v_mul_f32_e32 v204, v204, v128
	v_mfma_f32_32x32x16_f16 v[32:47], a[44:47], v[184:187], v[32:47]
	ds_read_b128 v[184:187], v192 offset:30720
	v_rcp_f32_e32 v206, v206
	v_mul_f32_e32 v205, v205, v129
	v_mfma_f32_32x32x16_f16 v[48:63], a[44:47], v[188:191], v[48:63]
	ds_read_b128 v[188:191], v192 offset:31744
	global_load_lds_dwordx4 v192, s[44:45] offset:2048 sc1
	v_rcp_f32_e32 v207, v207
	v_mul_f32_e32 v206, v206, v130
	s_waitcnt vmcnt(10)
	s_barrier
	s_waitcnt lgkmcnt(4)
	v_mfma_f32_32x32x16_f16 v[32:47], a[48:51], v[160:163], v[32:47]
	ds_read_b128 v[160:163], v192 offset:32768
	v_rcp_f32_e32 v208, v208
	v_mul_f32_e32 v207, v207, v131
	v_mfma_f32_32x32x16_f16 v[48:63], a[48:51], v[164:167], v[48:63]
	ds_read_b128 v[164:167], v192 offset:33792
	v_rcp_f32_e32 v209, v209
	v_fmamk_f32 v208, v208, 0xc0b8aa3b, v198
	v_mfma_f32_32x32x16_f16 v[32:47], a[52:55], v[168:171], v[32:47]
	ds_read_b128 v[168:171], v192 offset:34816
	v_rcp_f32_e32 v210, v210
	v_fmamk_f32 v209, v209, 0xc0b8aa3b, v198
	v_fma_f32 v128, v200, v208, v204
	v_mfma_f32_32x32x16_f16 v[48:63], a[52:55], v[172:175], v[48:63]
	ds_read_b128 v[172:175], v192 offset:35840
	global_load_lds_dwordx4 v192, s[44:45] offset:3072 sc1
	v_rcp_f32_e32 v211, v211
	v_fmamk_f32 v210, v210, 0xc0b8aa3b, v198
	v_fma_f32 v129, v201, v209, v205
	s_waitcnt lgkmcnt(4)
	v_mfma_f32_32x32x16_f16 v[32:47], a[56:59], v[176:179], v[32:47]
	ds_read_b128 v[176:179], v192 offset:36864
	v_rcp_f32_e32 v212, v212
	v_fmamk_f32 v211, v211, 0xc0b8aa3b, v198
	v_fma_f32 v130, v202, v210, v206
	v_mfma_f32_32x32x16_f16 v[48:63], a[56:59], v[180:183], v[48:63]
	ds_read_b128 v[180:183], v192 offset:37888
	v_rcp_f32_e32 v213, v213
	v_fma_f32 v131, v203, v211, v207
	v_mfma_f32_32x32x16_f16 v[32:47], a[60:63], v[184:187], v[32:47]
	ds_read_b128 v[184:187], v192 offset:38912
	v_rcp_f32_e32 v214, v214
	v_mfma_f32_32x32x16_f16 v[48:63], a[60:63], v[188:191], v[48:63]
	ds_read_b128 v[188:191], v192 offset:39936
	s_add_u32 s44, s34, 0x18000
	s_addc_u32 s45, s35, 0
	s_mov_b32 m0, s58
	s_nop 0
	global_load_lds_dwordx4 v192, s[44:45] sc1
	v_rcp_f32_e32 v215, v215
	s_waitcnt lgkmcnt(4)
	v_mfma_f32_32x32x16_f16 v[32:47], a[64:67], v[160:163], v[32:47]
	ds_read_b128 v[160:163], v192 offset:40960
	v_exp_f32_e32 v200, v128
	v_mfma_f32_32x32x16_f16 v[48:63], a[64:67], v[164:167], v[48:63]
	ds_read_b128 v[164:167], v192 offset:41984
	v_exp_f32_e32 v201, v129
	v_add_f32_e32 v200, 1.0, v200
	v_mfma_f32_32x32x16_f16 v[32:47], a[68:71], v[168:171], v[32:47]
	ds_read_b128 v[168:171], v192 offset:43008
	v_exp_f32_e32 v202, v130
	v_add_f32_e32 v201, 1.0, v201
	v_mfma_f32_32x32x16_f16 v[48:63], a[68:71], v[172:175], v[48:63]
	ds_read_b128 v[172:175], v192 offset:44032
	global_load_lds_dwordx4 v192, s[44:45] offset:1024 sc1
	v_exp_f32_e32 v203, v131
	v_add_f32_e32 v202, 1.0, v202
	s_waitcnt lgkmcnt(4)
	v_mfma_f32_32x32x16_f16 v[32:47], a[72:75], v[176:179], v[32:47]
	ds_read_b128 v[176:179], v192 offset:45056
	v_add_f32_e32 v203, 1.0, v203
	v_rcp_f32_e32 v200, v200
	v_mfma_f32_32x32x16_f16 v[48:63], a[72:75], v[180:183], v[48:63]
	ds_read_b128 v[180:183], v192 offset:46080
	v_rcp_f32_e32 v201, v201
	v_fma_f32 v200, v200, 2.0, -1.0
	v_mfma_f32_32x32x16_f16 v[32:47], a[76:79], v[184:187], v[32:47]
	ds_read_b128 v[184:187], v192 offset:47104
	v_rcp_f32_e32 v202, v202
	v_fma_f32 v201, v201, 2.0, -1.0
	v_mul_f32_e32 v216, v212, v200
	v_mfma_f32_32x32x16_f16 v[48:63], a[76:79], v[188:191], v[48:63]
	ds_read_b128 v[188:191], v192 offset:48128
	global_load_lds_dwordx4 v192, s[44:45] offset:2048 sc1
	v_rcp_f32_e32 v203, v203
	v_fma_f32 v202, v202, 2.0, -1.0
	v_mul_f32_e32 v217, v213, v201
	s_waitcnt lgkmcnt(4)
	v_mfma_f32_32x32x16_f16 v[32:47], a[80:83], v[160:163], v[32:47]
	ds_read_b128 v[160:163], v192 offset:49152
	v_fma_f32 v203, v203, 2.0, -1.0
	v_mul_f32_e32 v218, v214, v202
	v_exp_f32_e32 v200, v16
	v_mfma_f32_32x32x16_f16 v[48:63], a[80:83], v[164:167], v[48:63]
	ds_read_b128 v[164:167], v192 offset:50176
	v_mul_f32_e32 v219, v215, v203
	v_cvt_pk_f16_f32 v220, v216, v217
	v_exp_f32_e32 v201, v17
	v_mfma_f32_32x32x16_f16 v[32:47], a[84:87], v[168:171], v[32:47]
	ds_read_b128 v[168:171], v192 offset:51200
	v_cvt_pk_f16_f32 v221, v218, v219
	v_exp_f32_e32 v202, v18
	v_add_f32_e32 v200, 1.0, v200
	v_mfma_f32_32x32x16_f16 v[48:63], a[84:87], v[172:175], v[48:63]
	ds_read_b128 v[172:175], v192 offset:52224
	global_load_lds_dwordx4 v192, s[44:45] offset:3072 sc1
	s_cmp_lg_u32 s33, s60
	s_cbranch_scc1 .LE_nht26
	s_add_u32 s46, s62, 0x0
	s_addc_u32 s47, s63, 0
	global_store_dwordx4 v250, v[216:219], s[46:47]
	s_waitcnt vmcnt(0)

.LE_join33:
	v_mfma_f32_32x32x16_f16 v[32:47], a[196:199], v[168:171], v[32:47]
	ds_read_b128 v[168:171], v193 offset:43008
	v_fma_f32 v126, v231, v243, v246
	v_fma_f32 v127, v231, v245, v247
	v_mfma_f32_32x32x16_f16 v[48:63], a[196:199], v[172:175], v[48:63]
	ds_read_b128 v[172:175], v193 offset:44032
	global_load_lds_dwordx4 v192, s[44:45] offset:1024 sc1
	v_fmac_f32_e32 v126, v230, v242
	v_fmac_f32_e32 v127, v230, v244
	s_waitcnt lgkmcnt(4)
	v_mfma_f32_32x32x16_f16 v[32:47], a[200:203], v[176:179], v[32:47]
	ds_read_b128 v[176:179], v193 offset:45056
	v_mfma_f32_32x32x16_f16 v[48:63], a[200:203], v[180:183], v[48:63]
	ds_read_b128 v[180:183], v193 offset:46080
	s_and_b32 s64, s33, 1
	s_lshl_b32 s64, s64, 22
	s_add_u32 s64, s64, s50
	s_add_u32 s64, s64, 0x20000
	s_add_u32 s36, s6, s64
	s_addc_u32 s37, s7, 0
	s_lshl_b32 s64, s33, 3
	s_add_u32 s64, s64, s29
	s_lshl_b32 s64, s64, 5
	s_add_u32 s64, s64, s30
	s_lshl_b32 s64, s64, 2
	s_add_u32 s40, s8, s64
	s_addc_u32 s41, s9, 0
	s_lshl_b32 s64, s61, 11
	s_lshl_b32 s65, s29, 8
	s_add_u32 s64, s64, s65
	s_lshl_b32 s64, s64, 3
	s_add_u32 s42, s12, s64
	s_addc_u32 s43, s13, 0
	v_mfma_f32_32x32x16_f16 v[32:47], a[204:207], v[184:187], v[32:47]
	ds_read_b128 v[184:187], v193 offset:47104
	v_mfma_f32_32x32x16_f16 v[48:63], a[204:207], v[188:191], v[48:63]
	ds_read_b128 v[188:191], v193 offset:48128
	global_load_lds_dwordx4 v192, s[44:45] offset:2048 sc1
	s_waitcnt lgkmcnt(4)
	v_mfma_f32_32x32x16_f16 v[32:47], a[208:211], v[160:163], v[32:47]
	ds_read_b128 v[160:163], v193 offset:49152
	v_mfma_f32_32x32x16_f16 v[48:63], a[208:211], v[164:167], v[48:63]
	ds_read_b128 v[164:167], v193 offset:50176
	v_mfma_f32_32x32x16_f16 v[32:47], a[212:215], v[168:171], v[32:47]
	ds_read_b128 v[168:171], v193 offset:51200
	v_mfma_f32_32x32x16_f16 v[48:63], a[212:215], v[172:175], v[48:63]
	ds_read_b128 v[172:175], v193 offset:52224
	global_load_lds_dwordx4 v192, s[44:45] offset:3072 sc1
	s_waitcnt lgkmcnt(4)
	v_mfma_f32_32x32x16_f16 v[32:47], a[216:219], v[176:179], v[32:47]
	ds_read_b128 v[176:179], v193 offset:53248
	v_mfma_f32_32x32x16_f16 v[48:63], a[216:219], v[180:183], v[48:63]
	ds_read_b128 v[180:183], v193 offset:54272
	v_mfma_f32_32x32x16_f16 v[32:47], a[220:223], v[184:187], v[32:47]
	ds_read_b128 v[184:187], v193 offset:55296
	v_mfma_f32_32x32x16_f16 v[48:63], a[220:223], v[188:191], v[48:63]
	ds_read_b128 v[188:191], v193 offset:56320
	s_add_u32 s44, s34, 0x9000
	s_addc_u32 s45, s35, 0
	s_mov_b32 m0, s55
	s_nop 0
	global_load_lds_dwordx4 v192, s[44:45] sc1
	s_waitcnt lgkmcnt(4)
	v_mfma_f32_32x32x16_f16 v[32:47], a[224:227], v[160:163], v[32:47]
	ds_read_b128 v[160:163], v193 offset:57344
	v_mfma_f32_32x32x16_f16 v[48:63], a[224:227], v[164:167], v[48:63]
	ds_read_b128 v[164:167], v193 offset:58368
	v_mfma_f32_32x32x16_f16 v[32:47], a[228:231], v[168:171], v[32:47]
	ds_read_b128 v[168:171], v193 offset:59392
	v_mfma_f32_32x32x16_f16 v[48:63], a[228:231], v[172:175], v[48:63]
	ds_read_b128 v[172:175], v193 offset:60416
	global_load_lds_dwordx4 v192, s[44:45] offset:1024 sc1
	s_waitcnt lgkmcnt(4)
	v_mfma_f32_32x32x16_f16 v[32:47], a[232:235], v[176:179], v[32:47]
	ds_read_b128 v[176:179], v193 offset:61440
	v_mfma_f32_32x32x16_f16 v[48:63], a[232:235], v[180:183], v[48:63]
	ds_read_b128 v[180:183], v193 offset:62464
	v_mfma_f32_32x32x16_f16 v[32:47], a[236:239], v[184:187], v[32:47]
	ds_read_b128 v[184:187], v193 offset:63488
	v_mfma_f32_32x32x16_f16 v[48:63], a[236:239], v[188:191], v[48:63]
	ds_read_b128 v[188:191], v193 offset:64512
	global_load_lds_dwordx4 v192, s[44:45] offset:2048 sc1
	s_waitcnt vmcnt(8)
	s_barrier
	s_waitcnt lgkmcnt(4)
	v_mfma_f32_32x32x16_f16 v[32:47], a[240:243], v[160:163], v[32:47]
	ds_read_b128 v[160:163], v192 offset:0
	v_mfma_f32_32x32x16_f16 v[48:63], a[240:243], v[164:167], v[48:63]
	ds_read_b128 v[164:167], v192 offset:1024
	v_mfma_f32_32x32x16_f16 v[32:47], a[244:247], v[168:171], v[32:47]
	ds_read_b128 v[168:171], v192 offset:2048
	v_mfma_f32_32x32x16_f16 v[48:63], a[244:247], v[172:175], v[48:63]
	ds_read_b128 v[172:175], v192 offset:3072
	global_load_lds_dwordx4 v192, s[44:45] offset:3072 sc1
	s_waitcnt lgkmcnt(4)
	v_mfma_f32_32x32x16_f16 v[32:47], a[248:251], v[176:179], v[32:47]
	ds_read_b128 v[176:179], v192 offset:4096
	v_mfma_f32_32x32x16_f16 v[48:63], a[248:251], v[180:183], v[48:63]
	ds_read_b128 v[180:183], v192 offset:5120
	v_mfma_f32_32x32x16_f16 v[32:47], a[252:255], v[184:187], v[32:47]
	ds_read_b128 v[184:187], v192 offset:6144
	v_mfma_f32_32x32x16_f16 v[48:63], a[252:255], v[188:191], v[48:63]
	ds_read_b128 v[188:191], v192 offset:7168
	s_add_u32 s44, s34, 0x10000
	s_addc_u32 s45, s35, 0
	s_mov_b32 m0, s56
	s_nop 0
	global_load_lds_dwordx4 v192, s[44:45] sc1
	s_nop 3
	global_load_dwordx2 v[228:229], v249, s[42:43] offset:0
	global_load_dwordx2 v[230:231], v249, s[42:43] offset:256
	s_waitcnt lgkmcnt(4)
	v_mfma_f32_32x32x16_f16 v[64:79], a[0:3], v[160:163], v[64:79]
	ds_read_b128 v[160:163], v192 offset:8192
	v_exp_f32_e32 v200, v32
	v_mfma_f32_32x32x16_f16 v[80:95], a[0:3], v[164:167], v[80:95]
	ds_read_b128 v[164:167], v192 offset:9216
	s_lshl_b32 s64, s71, 3
	s_add_u32 s64, s64, s29
	s_lshl_b32 s64, s64, 7
	s_add_u32 s38, s8, s64
	s_addc_u32 s39, s9, 0
	global_load_dword v251, v196, s[38:39] sc1
	v_exp_f32_e32 v201, v33
	v_add_f32_e32 v200, 1.0, v200
	v_mfma_f32_32x32x16_f16 v[64:79], a[4:7], v[168:171], v[64:79]
	ds_read_b128 v[168:171], v192 offset:10240
	v_exp_f32_e32 v202, v34
	v_add_f32_e32 v201, 1.0, v201
	v_mfma_f32_32x32x16_f16 v[80:95], a[4:7], v[172:175], v[80:95]
	ds_read_b128 v[172:175], v192 offset:11264
	global_load_lds_dwordx4 v192, s[44:45] offset:1024 sc1
	v_exp_f32_e32 v203, v35
	v_add_f32_e32 v202, 1.0, v202
	s_waitcnt lgkmcnt(4)
	v_mfma_f32_32x32x16_f16 v[64:79], a[8:11], v[176:179], v[64:79]
	ds_read_b128 v[176:179], v192 offset:12288
	v_exp_f32_e32 v204, v36
	v_add_f32_e32 v203, 1.0, v203
	v_mfma_f32_32x32x16_f16 v[80:95], a[8:11], v[180:183], v[80:95]
	ds_read_b128 v[180:183], v192 offset:13312
	v_exp_f32_e32 v205, v37
	v_add_f32_e32 v204, 1.0, v204
	v_mfma_f32_32x32x16_f16 v[64:79], a[12:15], v[184:187], v[64:79]
	ds_read_b128 v[184:187], v192 offset:14336
	v_exp_f32_e32 v206, v38
	v_add_f32_e32 v205, 1.0, v205
	v_mfma_f32_32x32x16_f16 v[80:95], a[12:15], v[188:191], v[80:95]
	ds_read_b128 v[188:191], v192 offset:15360
	global_load_lds_dwordx4 v192, s[44:45] offset:2048 sc1
	v_exp_f32_e32 v207, v39
	v_add_f32_e32 v206, 1.0, v206
	s_waitcnt lgkmcnt(4)
	v_mfma_f32_32x32x16_f16 v[64:79], a[16:19], v[160:163], v[64:79]
	ds_read_b128 v[160:163], v192 offset:16384
	v_exp_f32_e32 v208, v40
	v_add_f32_e32 v207, 1.0, v207
	v_mfma_f32_32x32x16_f16 v[80:95], a[16:19], v[164:167], v[80:95]
	ds_read_b128 v[164:167], v192 offset:17408
	v_exp_f32_e32 v209, v41
	v_add_f32_e32 v208, 1.0, v208
	v_mfma_f32_32x32x16_f16 v[64:79], a[20:23], v[168:171], v[64:79]
	ds_read_b128 v[168:171], v192 offset:18432
	v_exp_f32_e32 v210, v42
	v_add_f32_e32 v209, 1.0, v209
	v_mfma_f32_32x32x16_f16 v[80:95], a[20:23], v[172:175], v[80:95]
	ds_read_b128 v[172:175], v192 offset:19456
	global_load_lds_dwordx4 v192, s[44:45] offset:3072 sc1
	v_exp_f32_e32 v211, v43
	v_add_f32_e32 v210, 1.0, v210
	s_waitcnt lgkmcnt(4)
	v_mfma_f32_32x32x16_f16 v[64:79], a[24:27], v[176:179], v[64:79]
	ds_read_b128 v[176:179], v192 offset:20480
	v_exp_f32_e32 v212, v44
	v_add_f32_e32 v211, 1.0, v211
	v_mfma_f32_32x32x16_f16 v[80:95], a[24:27], v[180:183], v[80:95]
	ds_read_b128 v[180:183], v192 offset:21504
	v_exp_f32_e32 v213, v45
	v_add_f32_e32 v212, 1.0, v212
	v_mfma_f32_32x32x16_f16 v[64:79], a[28:31], v[184:187], v[64:79]
	ds_read_b128 v[184:187], v192 offset:22528
	v_exp_f32_e32 v214, v46
	v_add_f32_e32 v213, 1.0, v213
	v_mfma_f32_32x32x16_f16 v[80:95], a[28:31], v[188:191], v[80:95]
	ds_read_b128 v[188:191], v192 offset:23552
	s_add_u32 s44, s34, 0x11000
	s_addc_u32 s45, s35, 0
	s_mov_b32 m0, s57
	s_nop 0
	global_load_lds_dwordx4 v192, s[44:45] sc1
	v_exp_f32_e32 v215, v47
	v_add_f32_e32 v214, 1.0, v214
	s_waitcnt lgkmcnt(4)
	v_mfma_f32_32x32x16_f16 v[64:79], a[32:35], v[160:163], v[64:79]
	ds_read_b128 v[160:163], v192 offset:24576
	v_add_f32_e32 v215, 1.0, v215
	v_rcp_f32_e32 v200, v200
	v_mfma_f32_32x32x16_f16 v[80:95], a[32:35], v[164:167], v[80:95]
	ds_read_b128 v[164:167], v192 offset:25600
	v_rcp_f32_e32 v201, v201
	v_mfma_f32_32x32x16_f16 v[64:79], a[36:39], v[168:171], v[64:79]
	ds_read_b128 v[168:171], v192 offset:26624
	v_rcp_f32_e32 v202, v202
	v_mfma_f32_32x32x16_f16 v[80:95], a[36:39], v[172:175], v[80:95]
	ds_read_b128 v[172:175], v192 offset:27648
	global_load_lds_dwordx4 v192, s[44:45] offset:1024 sc1
	v_rcp_f32_e32 v203, v203
	s_waitcnt lgkmcnt(4)
	v_mfma_f32_32x32x16_f16 v[64:79], a[40:43], v[176:179], v[64:79]
	ds_read_b128 v[176:179], v192 offset:28672
	v_rcp_f32_e32 v204, v204
	v_mfma_f32_32x32x16_f16 v[80:95], a[40:43], v[180:183], v[80:95]
	ds_read_b128 v[180:183], v192 offset:29696
	v_rcp_f32_e32 v205, v205
	v_mul_f32_e32 v204, v204, v136
	v_mfma_f32_32x32x16_f16 v[64:79], a[44:47], v[184:187], v[64:79]
	ds_read_b128 v[184:187], v192 offset:30720
	v_rcp_f32_e32 v206, v206
	v_mul_f32_e32 v205, v205, v137
	v_mfma_f32_32x32x16_f16 v[80:95], a[44:47], v[188:191], v[80:95]
	ds_read_b128 v[188:191], v192 offset:31744
	global_load_lds_dwordx4 v192, s[44:45] offset:2048 sc1
	v_rcp_f32_e32 v207, v207
	v_mul_f32_e32 v206, v206, v138
	s_waitcnt vmcnt(10)
	s_barrier
	s_waitcnt lgkmcnt(4)
	v_mfma_f32_32x32x16_f16 v[64:79], a[48:51], v[160:163], v[64:79]
	ds_read_b128 v[160:163], v192 offset:32768
	v_rcp_f32_e32 v208, v208
	v_mul_f32_e32 v207, v207, v139
	v_mfma_f32_32x32x16_f16 v[80:95], a[48:51], v[164:167], v[80:95]
	ds_read_b128 v[164:167], v192 offset:33792
	v_rcp_f32_e32 v209, v209
	v_fmamk_f32 v208, v208, 0xc0b8aa3b, v198
	v_mfma_f32_32x32x16_f16 v[64:79], a[52:55], v[168:171], v[64:79]
	ds_read_b128 v[168:171], v192 offset:34816
	v_rcp_f32_e32 v210, v210
	v_fmamk_f32 v209, v209, 0xc0b8aa3b, v198
	v_fma_f32 v136, v200, v208, v204
	v_mfma_f32_32x32x16_f16 v[80:95], a[52:55], v[172:175], v[80:95]
	ds_read_b128 v[172:175], v192 offset:35840
	global_load_lds_dwordx4 v192, s[44:45] offset:3072 sc1
	v_rcp_f32_e32 v211, v211
	v_fmamk_f32 v210, v210, 0xc0b8aa3b, v198
	v_fma_f32 v137, v201, v209, v205
	s_waitcnt lgkmcnt(4)
	v_mfma_f32_32x32x16_f16 v[64:79], a[56:59], v[176:179], v[64:79]
	ds_read_b128 v[176:179], v192 offset:36864
	v_rcp_f32_e32 v212, v212
	v_fmamk_f32 v211, v211, 0xc0b8aa3b, v198
	v_fma_f32 v138, v202, v210, v206
	v_mfma_f32_32x32x16_f16 v[80:95], a[56:59], v[180:183], v[80:95]
	ds_read_b128 v[180:183], v192 offset:37888
	v_rcp_f32_e32 v213, v213
	v_fma_f32 v139, v203, v211, v207
	v_mfma_f32_32x32x16_f16 v[64:79], a[60:63], v[184:187], v[64:79]
	ds_read_b128 v[184:187], v192 offset:38912
	v_rcp_f32_e32 v214, v214
	v_mfma_f32_32x32x16_f16 v[80:95], a[60:63], v[188:191], v[80:95]
	ds_read_b128 v[188:191], v192 offset:39936
	s_add_u32 s44, s34, 0x18000
	s_addc_u32 s45, s35, 0
	s_mov_b32 m0, s58
	s_nop 0
	global_load_lds_dwordx4 v192, s[44:45] sc1
	v_rcp_f32_e32 v215, v215
	s_waitcnt lgkmcnt(4)
	v_mfma_f32_32x32x16_f16 v[64:79], a[64:67], v[160:163], v[64:79]
	ds_read_b128 v[160:163], v192 offset:40960
	v_exp_f32_e32 v200, v136
	v_mfma_f32_32x32x16_f16 v[80:95], a[64:67], v[164:167], v[80:95]
	ds_read_b128 v[164:167], v192 offset:41984
	v_exp_f32_e32 v201, v137
	v_add_f32_e32 v200, 1.0, v200
	v_mfma_f32_32x32x16_f16 v[64:79], a[68:71], v[168:171], v[64:79]
	ds_read_b128 v[168:171], v192 offset:43008
	v_exp_f32_e32 v202, v138
	v_add_f32_e32 v201, 1.0, v201
	v_mfma_f32_32x32x16_f16 v[80:95], a[68:71], v[172:175], v[80:95]
	ds_read_b128 v[172:175], v192 offset:44032
	global_load_lds_dwordx4 v192, s[44:45] offset:1024 sc1
	v_exp_f32_e32 v203, v139
	v_add_f32_e32 v202, 1.0, v202
	s_waitcnt lgkmcnt(4)
	v_mfma_f32_32x32x16_f16 v[64:79], a[72:75], v[176:179], v[64:79]
	ds_read_b128 v[176:179], v192 offset:45056
	v_add_f32_e32 v203, 1.0, v203
	v_rcp_f32_e32 v200, v200
	v_mfma_f32_32x32x16_f16 v[80:95], a[72:75], v[180:183], v[80:95]
	ds_read_b128 v[180:183], v192 offset:46080
	v_rcp_f32_e32 v201, v201
	v_fma_f32 v200, v200, 2.0, -1.0
	v_mfma_f32_32x32x16_f16 v[64:79], a[76:79], v[184:187], v[64:79]
	ds_read_b128 v[184:187], v192 offset:47104
	v_rcp_f32_e32 v202, v202
	v_fma_f32 v201, v201, 2.0, -1.0
	v_mul_f32_e32 v216, v212, v200
	v_mfma_f32_32x32x16_f16 v[80:95], a[76:79], v[188:191], v[80:95]
	ds_read_b128 v[188:191], v192 offset:48128
	global_load_lds_dwordx4 v192, s[44:45] offset:2048 sc1
	v_rcp_f32_e32 v203, v203
	v_fma_f32 v202, v202, 2.0, -1.0
	v_mul_f32_e32 v217, v213, v201
	s_waitcnt lgkmcnt(4)
	v_mfma_f32_32x32x16_f16 v[64:79], a[80:83], v[160:163], v[64:79]
	ds_read_b128 v[160:163], v192 offset:49152
	v_fma_f32 v203, v203, 2.0, -1.0
	v_mul_f32_e32 v218, v214, v202
	v_exp_f32_e32 v200, v48
	v_mfma_f32_32x32x16_f16 v[80:95], a[80:83], v[164:167], v[80:95]
	ds_read_b128 v[164:167], v192 offset:50176
	v_mul_f32_e32 v219, v215, v203
	v_cvt_pk_f16_f32 v220, v216, v217
	v_exp_f32_e32 v201, v49
	v_mfma_f32_32x32x16_f16 v[64:79], a[84:87], v[168:171], v[64:79]
	ds_read_b128 v[168:171], v192 offset:51200
	v_cvt_pk_f16_f32 v221, v218, v219
	v_exp_f32_e32 v202, v50
	v_add_f32_e32 v200, 1.0, v200
	v_mfma_f32_32x32x16_f16 v[80:95], a[84:87], v[172:175], v[80:95]
	ds_read_b128 v[172:175], v192 offset:52224
	global_load_lds_dwordx4 v192, s[44:45] offset:3072 sc1
	s_cmp_lg_u32 s33, s60
	s_cbranch_scc1 .LE_nht34
	s_add_u32 s46, s62, 0x40000
	s_addc_u32 s47, s63, 0
	global_store_dwordx4 v250, v[216:219], s[46:47]
	s_waitcnt vmcnt(0)

.LE_join41:
	v_mfma_f32_32x32x16_f16 v[64:79], a[196:199], v[168:171], v[64:79]
	ds_read_b128 v[168:171], v193 offset:43008
	v_fma_f32 v30, v231, v243, v246
	v_fma_f32 v31, v231, v245, v247
	v_mfma_f32_32x32x16_f16 v[80:95], a[196:199], v[172:175], v[80:95]
	ds_read_b128 v[172:175], v193 offset:44032
	global_load_lds_dwordx4 v192, s[44:45] offset:1024 sc1
	v_fmac_f32_e32 v30, v230, v242
	v_fmac_f32_e32 v31, v230, v244
	s_waitcnt lgkmcnt(4)
	v_mfma_f32_32x32x16_f16 v[64:79], a[200:203], v[176:179], v[64:79]
	ds_read_b128 v[176:179], v193 offset:45056
	v_mfma_f32_32x32x16_f16 v[80:95], a[200:203], v[180:183], v[80:95]
	ds_read_b128 v[180:183], v193 offset:46080
	s_and_b32 s64, s33, 1
	s_lshl_b32 s64, s64, 22
	s_add_u32 s64, s64, s50
	s_add_u32 s64, s64, 0x40000
	s_add_u32 s36, s6, s64
	s_addc_u32 s37, s7, 0
	s_lshl_b32 s64, s33, 3
	s_add_u32 s64, s64, s29
	s_lshl_b32 s64, s64, 5
	s_add_u32 s64, s64, s30
	s_lshl_b32 s64, s64, 2
	s_add_u32 s40, s8, s64
	s_addc_u32 s41, s9, 0
	s_lshl_b32 s64, s61, 11
	s_lshl_b32 s65, s29, 8
	s_add_u32 s64, s64, s65
	s_add_u32 s64, s64, 64
	s_lshl_b32 s64, s64, 3
	s_add_u32 s42, s12, s64
	s_addc_u32 s43, s13, 0
	v_mfma_f32_32x32x16_f16 v[64:79], a[204:207], v[184:187], v[64:79]
	ds_read_b128 v[184:187], v193 offset:47104
	v_mfma_f32_32x32x16_f16 v[80:95], a[204:207], v[188:191], v[80:95]
	ds_read_b128 v[188:191], v193 offset:48128
	global_load_lds_dwordx4 v192, s[44:45] offset:2048 sc1
	s_waitcnt lgkmcnt(4)
	v_mfma_f32_32x32x16_f16 v[64:79], a[208:211], v[160:163], v[64:79]
	ds_read_b128 v[160:163], v193 offset:49152
	v_mfma_f32_32x32x16_f16 v[80:95], a[208:211], v[164:167], v[80:95]
	ds_read_b128 v[164:167], v193 offset:50176
	v_mfma_f32_32x32x16_f16 v[64:79], a[212:215], v[168:171], v[64:79]
	ds_read_b128 v[168:171], v193 offset:51200
	v_mfma_f32_32x32x16_f16 v[80:95], a[212:215], v[172:175], v[80:95]
	ds_read_b128 v[172:175], v193 offset:52224
	global_load_lds_dwordx4 v192, s[44:45] offset:3072 sc1
	s_waitcnt lgkmcnt(4)
	v_mfma_f32_32x32x16_f16 v[64:79], a[216:219], v[176:179], v[64:79]
	ds_read_b128 v[176:179], v193 offset:53248
	v_mfma_f32_32x32x16_f16 v[80:95], a[216:219], v[180:183], v[80:95]
	ds_read_b128 v[180:183], v193 offset:54272
	v_mfma_f32_32x32x16_f16 v[64:79], a[220:223], v[184:187], v[64:79]
	ds_read_b128 v[184:187], v193 offset:55296
	v_mfma_f32_32x32x16_f16 v[80:95], a[220:223], v[188:191], v[80:95]
	ds_read_b128 v[188:191], v193 offset:56320
	s_add_u32 s44, s34, 0x9000
	s_addc_u32 s45, s35, 0
	s_mov_b32 m0, s55
	s_nop 0
	global_load_lds_dwordx4 v192, s[44:45] sc1
	s_waitcnt lgkmcnt(4)
	v_mfma_f32_32x32x16_f16 v[64:79], a[224:227], v[160:163], v[64:79]
	ds_read_b128 v[160:163], v193 offset:57344
	v_mfma_f32_32x32x16_f16 v[80:95], a[224:227], v[164:167], v[80:95]
	ds_read_b128 v[164:167], v193 offset:58368
	v_mfma_f32_32x32x16_f16 v[64:79], a[228:231], v[168:171], v[64:79]
	ds_read_b128 v[168:171], v193 offset:59392
	v_mfma_f32_32x32x16_f16 v[80:95], a[228:231], v[172:175], v[80:95]
	ds_read_b128 v[172:175], v193 offset:60416
	global_load_lds_dwordx4 v192, s[44:45] offset:1024 sc1
	s_waitcnt lgkmcnt(4)
	v_mfma_f32_32x32x16_f16 v[64:79], a[232:235], v[176:179], v[64:79]
	ds_read_b128 v[176:179], v193 offset:61440
	v_mfma_f32_32x32x16_f16 v[80:95], a[232:235], v[180:183], v[80:95]
	ds_read_b128 v[180:183], v193 offset:62464
	v_mfma_f32_32x32x16_f16 v[64:79], a[236:239], v[184:187], v[64:79]
	ds_read_b128 v[184:187], v193 offset:63488
	v_mfma_f32_32x32x16_f16 v[80:95], a[236:239], v[188:191], v[80:95]
	ds_read_b128 v[188:191], v193 offset:64512
	global_load_lds_dwordx4 v192, s[44:45] offset:2048 sc1
	s_waitcnt vmcnt(8)
	s_barrier
	s_waitcnt lgkmcnt(4)
	v_mfma_f32_32x32x16_f16 v[64:79], a[240:243], v[160:163], v[64:79]
	ds_read_b128 v[160:163], v192 offset:0
	v_mfma_f32_32x32x16_f16 v[80:95], a[240:243], v[164:167], v[80:95]
	ds_read_b128 v[164:167], v192 offset:1024
	v_mfma_f32_32x32x16_f16 v[64:79], a[244:247], v[168:171], v[64:79]
	ds_read_b128 v[168:171], v192 offset:2048
	v_mfma_f32_32x32x16_f16 v[80:95], a[244:247], v[172:175], v[80:95]
	ds_read_b128 v[172:175], v192 offset:3072
	global_load_lds_dwordx4 v192, s[44:45] offset:3072 sc1
	s_waitcnt lgkmcnt(4)
	v_mfma_f32_32x32x16_f16 v[64:79], a[248:251], v[176:179], v[64:79]
	ds_read_b128 v[176:179], v192 offset:4096
	v_mfma_f32_32x32x16_f16 v[80:95], a[248:251], v[180:183], v[80:95]
	ds_read_b128 v[180:183], v192 offset:5120
	v_mfma_f32_32x32x16_f16 v[64:79], a[252:255], v[184:187], v[64:79]
	ds_read_b128 v[184:187], v192 offset:6144
	v_mfma_f32_32x32x16_f16 v[80:95], a[252:255], v[188:191], v[80:95]
	ds_read_b128 v[188:191], v192 offset:7168
	s_add_u32 s44, s34, 0x10000
	s_addc_u32 s45, s35, 0
	s_mov_b32 m0, s56
	s_nop 0
	global_load_lds_dwordx4 v192, s[44:45] sc1
	s_nop 3
	global_load_dwordx2 v[228:229], v249, s[42:43] offset:0
	global_load_dwordx2 v[230:231], v249, s[42:43] offset:256
	s_waitcnt lgkmcnt(4)
	v_mfma_f32_32x32x16_f16 v[96:111], a[0:3], v[160:163], v[96:111]
	ds_read_b128 v[160:163], v192 offset:8192
	v_exp_f32_e32 v200, v64
	v_mfma_f32_32x32x16_f16 v[112:127], a[0:3], v[164:167], v[112:127]
	ds_read_b128 v[164:167], v192 offset:9216
	s_lshl_b32 s64, s33, 3
	s_add_u32 s64, s64, s29
	s_lshl_b32 s64, s64, 7
	s_add_u32 s38, s8, s64
	s_addc_u32 s39, s9, 0
	global_load_dword v251, v196, s[38:39] sc1
	v_exp_f32_e32 v201, v65
	v_add_f32_e32 v200, 1.0, v200
	v_mfma_f32_32x32x16_f16 v[96:111], a[4:7], v[168:171], v[96:111]
	ds_read_b128 v[168:171], v192 offset:10240
	v_exp_f32_e32 v202, v66
	v_add_f32_e32 v201, 1.0, v201
	v_mfma_f32_32x32x16_f16 v[112:127], a[4:7], v[172:175], v[112:127]
	ds_read_b128 v[172:175], v192 offset:11264
	global_load_lds_dwordx4 v192, s[44:45] offset:1024 sc1
	v_exp_f32_e32 v203, v67
	v_add_f32_e32 v202, 1.0, v202
	s_waitcnt lgkmcnt(4)
	v_mfma_f32_32x32x16_f16 v[96:111], a[8:11], v[176:179], v[96:111]
	ds_read_b128 v[176:179], v192 offset:12288
	v_exp_f32_e32 v204, v68
	v_add_f32_e32 v203, 1.0, v203
	v_mfma_f32_32x32x16_f16 v[112:127], a[8:11], v[180:183], v[112:127]
	ds_read_b128 v[180:183], v192 offset:13312
	v_exp_f32_e32 v205, v69
	v_add_f32_e32 v204, 1.0, v204
	v_mfma_f32_32x32x16_f16 v[96:111], a[12:15], v[184:187], v[96:111]
	ds_read_b128 v[184:187], v192 offset:14336
	v_exp_f32_e32 v206, v70
	v_add_f32_e32 v205, 1.0, v205
	v_mfma_f32_32x32x16_f16 v[112:127], a[12:15], v[188:191], v[112:127]
	ds_read_b128 v[188:191], v192 offset:15360
	global_load_lds_dwordx4 v192, s[44:45] offset:2048 sc1
	v_exp_f32_e32 v207, v71
	v_add_f32_e32 v206, 1.0, v206
	s_waitcnt lgkmcnt(4)
	v_mfma_f32_32x32x16_f16 v[96:111], a[16:19], v[160:163], v[96:111]
	ds_read_b128 v[160:163], v192 offset:16384
	v_exp_f32_e32 v208, v72
	v_add_f32_e32 v207, 1.0, v207
	v_mfma_f32_32x32x16_f16 v[112:127], a[16:19], v[164:167], v[112:127]
	ds_read_b128 v[164:167], v192 offset:17408
	v_exp_f32_e32 v209, v73
	v_add_f32_e32 v208, 1.0, v208
	v_mfma_f32_32x32x16_f16 v[96:111], a[20:23], v[168:171], v[96:111]
	ds_read_b128 v[168:171], v192 offset:18432
	v_exp_f32_e32 v210, v74
	v_add_f32_e32 v209, 1.0, v209
	v_mfma_f32_32x32x16_f16 v[112:127], a[20:23], v[172:175], v[112:127]
	ds_read_b128 v[172:175], v192 offset:19456
	global_load_lds_dwordx4 v192, s[44:45] offset:3072 sc1
	v_exp_f32_e32 v211, v75
	v_add_f32_e32 v210, 1.0, v210
	s_waitcnt lgkmcnt(4)
	v_mfma_f32_32x32x16_f16 v[96:111], a[24:27], v[176:179], v[96:111]
	ds_read_b128 v[176:179], v192 offset:20480
	v_exp_f32_e32 v212, v76
	v_add_f32_e32 v211, 1.0, v211
	v_mfma_f32_32x32x16_f16 v[112:127], a[24:27], v[180:183], v[112:127]
	ds_read_b128 v[180:183], v192 offset:21504
	v_exp_f32_e32 v213, v77
	v_add_f32_e32 v212, 1.0, v212
	v_mfma_f32_32x32x16_f16 v[96:111], a[28:31], v[184:187], v[96:111]
	ds_read_b128 v[184:187], v192 offset:22528
	v_exp_f32_e32 v214, v78
	v_add_f32_e32 v213, 1.0, v213
	v_mfma_f32_32x32x16_f16 v[112:127], a[28:31], v[188:191], v[112:127]
	ds_read_b128 v[188:191], v192 offset:23552
	s_add_u32 s44, s34, 0x11000
	s_addc_u32 s45, s35, 0
	s_mov_b32 m0, s57
	s_nop 0
	global_load_lds_dwordx4 v192, s[44:45] sc1
	v_exp_f32_e32 v215, v79
	v_add_f32_e32 v214, 1.0, v214
	s_waitcnt lgkmcnt(4)
	v_mfma_f32_32x32x16_f16 v[96:111], a[32:35], v[160:163], v[96:111]
	ds_read_b128 v[160:163], v192 offset:24576
	v_add_f32_e32 v215, 1.0, v215
	v_rcp_f32_e32 v200, v200
	v_mfma_f32_32x32x16_f16 v[112:127], a[32:35], v[164:167], v[112:127]
	ds_read_b128 v[164:167], v192 offset:25600
	v_rcp_f32_e32 v201, v201
	v_mfma_f32_32x32x16_f16 v[96:111], a[36:39], v[168:171], v[96:111]
	ds_read_b128 v[168:171], v192 offset:26624
	v_rcp_f32_e32 v202, v202
	v_mfma_f32_32x32x16_f16 v[112:127], a[36:39], v[172:175], v[112:127]
	ds_read_b128 v[172:175], v192 offset:27648
	global_load_lds_dwordx4 v192, s[44:45] offset:1024 sc1
	v_rcp_f32_e32 v203, v203
	s_waitcnt lgkmcnt(4)
	v_mfma_f32_32x32x16_f16 v[96:111], a[40:43], v[176:179], v[96:111]
	ds_read_b128 v[176:179], v192 offset:28672
	v_rcp_f32_e32 v204, v204
	v_mfma_f32_32x32x16_f16 v[112:127], a[40:43], v[180:183], v[112:127]
	ds_read_b128 v[180:183], v192 offset:29696
	v_rcp_f32_e32 v205, v205
	v_mul_f32_e32 v204, v204, v144
	v_mfma_f32_32x32x16_f16 v[96:111], a[44:47], v[184:187], v[96:111]
	ds_read_b128 v[184:187], v192 offset:30720
	v_rcp_f32_e32 v206, v206
	v_mul_f32_e32 v205, v205, v145
	v_mfma_f32_32x32x16_f16 v[112:127], a[44:47], v[188:191], v[112:127]
	ds_read_b128 v[188:191], v192 offset:31744
	global_load_lds_dwordx4 v192, s[44:45] offset:2048 sc1
	v_rcp_f32_e32 v207, v207
	v_mul_f32_e32 v206, v206, v146
	s_waitcnt vmcnt(10)
	s_barrier
	s_waitcnt lgkmcnt(4)
	v_mfma_f32_32x32x16_f16 v[96:111], a[48:51], v[160:163], v[96:111]
	ds_read_b128 v[160:163], v192 offset:32768
	v_rcp_f32_e32 v208, v208
	v_mul_f32_e32 v207, v207, v147
	v_mfma_f32_32x32x16_f16 v[112:127], a[48:51], v[164:167], v[112:127]
	ds_read_b128 v[164:167], v192 offset:33792
	v_rcp_f32_e32 v209, v209
	v_fmamk_f32 v208, v208, 0xc0b8aa3b, v198
	v_mfma_f32_32x32x16_f16 v[96:111], a[52:55], v[168:171], v[96:111]
	ds_read_b128 v[168:171], v192 offset:34816
	v_rcp_f32_e32 v210, v210
	v_fmamk_f32 v209, v209, 0xc0b8aa3b, v198
	v_fma_f32 v144, v200, v208, v204
	v_mfma_f32_32x32x16_f16 v[112:127], a[52:55], v[172:175], v[112:127]
	ds_read_b128 v[172:175], v192 offset:35840
	global_load_lds_dwordx4 v192, s[44:45] offset:3072 sc1
	v_rcp_f32_e32 v211, v211
	v_fmamk_f32 v210, v210, 0xc0b8aa3b, v198
	v_fma_f32 v145, v201, v209, v205
	s_waitcnt lgkmcnt(4)
	v_mfma_f32_32x32x16_f16 v[96:111], a[56:59], v[176:179], v[96:111]
	ds_read_b128 v[176:179], v192 offset:36864
	v_rcp_f32_e32 v212, v212
	v_fmamk_f32 v211, v211, 0xc0b8aa3b, v198
	v_fma_f32 v146, v202, v210, v206
	v_mfma_f32_32x32x16_f16 v[112:127], a[56:59], v[180:183], v[112:127]
	ds_read_b128 v[180:183], v192 offset:37888
	v_rcp_f32_e32 v213, v213
	v_fma_f32 v147, v203, v211, v207
	v_mfma_f32_32x32x16_f16 v[96:111], a[60:63], v[184:187], v[96:111]
	ds_read_b128 v[184:187], v192 offset:38912
	v_rcp_f32_e32 v214, v214
	v_mfma_f32_32x32x16_f16 v[112:127], a[60:63], v[188:191], v[112:127]
	ds_read_b128 v[188:191], v192 offset:39936
	s_add_u32 s44, s34, 0x18000
	s_addc_u32 s45, s35, 0
	s_mov_b32 m0, s58
	s_nop 0
	global_load_lds_dwordx4 v192, s[44:45] sc1
	v_rcp_f32_e32 v215, v215
	s_waitcnt lgkmcnt(4)
	v_mfma_f32_32x32x16_f16 v[96:111], a[64:67], v[160:163], v[96:111]
	ds_read_b128 v[160:163], v192 offset:40960
	v_exp_f32_e32 v200, v144
	v_mfma_f32_32x32x16_f16 v[112:127], a[64:67], v[164:167], v[112:127]
	ds_read_b128 v[164:167], v192 offset:41984
	v_exp_f32_e32 v201, v145
	v_add_f32_e32 v200, 1.0, v200
	v_mfma_f32_32x32x16_f16 v[96:111], a[68:71], v[168:171], v[96:111]
	ds_read_b128 v[168:171], v192 offset:43008
	v_exp_f32_e32 v202, v146
	v_add_f32_e32 v201, 1.0, v201
	v_mfma_f32_32x32x16_f16 v[112:127], a[68:71], v[172:175], v[112:127]
	ds_read_b128 v[172:175], v192 offset:44032
	global_load_lds_dwordx4 v192, s[44:45] offset:1024 sc1
	v_exp_f32_e32 v203, v147
	v_add_f32_e32 v202, 1.0, v202
	s_waitcnt lgkmcnt(4)
	v_mfma_f32_32x32x16_f16 v[96:111], a[72:75], v[176:179], v[96:111]
	ds_read_b128 v[176:179], v192 offset:45056
	v_add_f32_e32 v203, 1.0, v203
	v_rcp_f32_e32 v200, v200
	v_mfma_f32_32x32x16_f16 v[112:127], a[72:75], v[180:183], v[112:127]
	ds_read_b128 v[180:183], v192 offset:46080
	v_rcp_f32_e32 v201, v201
	v_fma_f32 v200, v200, 2.0, -1.0
	v_mfma_f32_32x32x16_f16 v[96:111], a[76:79], v[184:187], v[96:111]
	ds_read_b128 v[184:187], v192 offset:47104
	v_rcp_f32_e32 v202, v202
	v_fma_f32 v201, v201, 2.0, -1.0
	v_mul_f32_e32 v216, v212, v200
	v_mfma_f32_32x32x16_f16 v[112:127], a[76:79], v[188:191], v[112:127]
	ds_read_b128 v[188:191], v192 offset:48128
	global_load_lds_dwordx4 v192, s[44:45] offset:2048 sc1
	v_rcp_f32_e32 v203, v203
	v_fma_f32 v202, v202, 2.0, -1.0
	v_mul_f32_e32 v217, v213, v201
	s_waitcnt lgkmcnt(4)
	v_mfma_f32_32x32x16_f16 v[96:111], a[80:83], v[160:163], v[96:111]
	ds_read_b128 v[160:163], v192 offset:49152
	v_fma_f32 v203, v203, 2.0, -1.0
	v_mul_f32_e32 v218, v214, v202
	v_exp_f32_e32 v200, v80
	v_mfma_f32_32x32x16_f16 v[112:127], a[80:83], v[164:167], v[112:127]
	ds_read_b128 v[164:167], v192 offset:50176
	v_mul_f32_e32 v219, v215, v203
	v_cvt_pk_f16_f32 v220, v216, v217
	v_exp_f32_e32 v201, v81
	v_mfma_f32_32x32x16_f16 v[96:111], a[84:87], v[168:171], v[96:111]
	ds_read_b128 v[168:171], v192 offset:51200
	v_cvt_pk_f16_f32 v221, v218, v219
	v_exp_f32_e32 v202, v82
	v_add_f32_e32 v200, 1.0, v200
	v_mfma_f32_32x32x16_f16 v[112:127], a[84:87], v[172:175], v[112:127]
	ds_read_b128 v[172:175], v192 offset:52224
	global_load_lds_dwordx4 v192, s[44:45] offset:3072 sc1
	s_cmp_lg_u32 s33, s60
	s_cbranch_scc1 .LE_nht42
	s_add_u32 s46, s62, 0x80000
	s_addc_u32 s47, s63, 0
	global_store_dwordx4 v250, v[216:219], s[46:47]
	s_waitcnt vmcnt(0)

.LD_join25:
	ds_read_b64 v[200:201], v249 offset:1536
	ds_read_b64 v[202:203], v249 offset:3584
	ds_read_b64 v[204:205], v249 offset:5632
	ds_read_b64 v[206:207], v249 offset:7680
	s_waitcnt lgkmcnt(8)
	v_mfma_f32_32x32x16_f16 v[0:15], a[208:211], v[160:163], v[0:15]
	ds_read_b128 v[160:163], v193 offset:49152
	v_mfma_f32_32x32x16_f16 v[16:31], a[208:211], v[164:167], v[16:31]
	ds_read_b128 v[164:167], v193 offset:50176
	v_mfma_f32_32x32x16_f16 v[0:15], a[212:215], v[168:171], v[0:15]
	ds_read_b128 v[168:171], v193 offset:51200
	v_mfma_f32_32x32x16_f16 v[16:31], a[212:215], v[172:175], v[16:31]
	ds_read_b128 v[172:175], v193 offset:52224
	global_load_lds_dwordx4 v192, s[44:45] offset:3072 sc1
	s_waitcnt lgkmcnt(8)
	v_mfma_f32_32x32x16_f16 v[0:15], a[216:219], v[176:179], v[0:15]
	ds_read_b128 v[176:179], v193 offset:53248
	v_mfma_f32_32x32x16_f16 v[16:31], a[216:219], v[180:183], v[16:31]
	ds_read_b128 v[180:183], v193 offset:54272
	v_mfma_f32_32x32x16_f16 v[0:15], a[220:223], v[184:187], v[0:15]
	ds_read_b128 v[184:187], v193 offset:55296
	v_mfma_f32_32x32x16_f16 v[16:31], a[220:223], v[188:191], v[16:31]
	ds_read_b128 v[188:191], v193 offset:56320
	s_add_u32 s44, s34, 0x9000
	s_addc_u32 s45, s35, 0
	s_mov_b32 m0, s55
	s_nop 0
	global_load_lds_dwordx4 v192, s[44:45] sc1
	s_waitcnt lgkmcnt(4)
	v_mfma_f32_32x32x16_f16 v[0:15], a[224:227], v[160:163], v[0:15]
	ds_read_b128 v[160:163], v193 offset:57344
	v_mfma_f32_32x32x16_f16 v[16:31], a[224:227], v[164:167], v[16:31]
	ds_read_b128 v[164:167], v193 offset:58368
	v_mfma_f32_32x32x16_f16 v[0:15], a[228:231], v[168:171], v[0:15]
	ds_read_b128 v[168:171], v193 offset:59392
	v_mfma_f32_32x32x16_f16 v[16:31], a[228:231], v[172:175], v[16:31]
	ds_read_b128 v[172:175], v193 offset:60416
	global_load_lds_dwordx4 v192, s[44:45] offset:1024 sc1
	v_add_f32_e32 v200, v200, v202
	v_add_f32_e32 v201, v201, v203
	v_add_f32_e32 v200, v200, v204
	v_add_f32_e32 v201, v201, v205
	v_add_f32_e32 v200, v200, v206
	v_add_f32_e32 v201, v201, v207
	global_store_dwordx2 v250, v[200:201], s[72:73]
	s_waitcnt lgkmcnt(4)
	v_mfma_f32_32x32x16_f16 v[0:15], a[232:235], v[176:179], v[0:15]
	ds_read_b128 v[176:179], v193 offset:61440
	v_mfma_f32_32x32x16_f16 v[16:31], a[232:235], v[180:183], v[16:31]
	ds_read_b128 v[180:183], v193 offset:62464
	v_mfma_f32_32x32x16_f16 v[0:15], a[236:239], v[184:187], v[0:15]
	ds_read_b128 v[184:187], v193 offset:63488
	v_mfma_f32_32x32x16_f16 v[16:31], a[236:239], v[188:191], v[16:31]
	ds_read_b128 v[188:191], v193 offset:64512
	global_load_lds_dwordx4 v192, s[44:45] offset:2048 sc1
	s_and_b32 s64, s33, 1
	s_lshl_b32 s64, s64, 22
	s_add_u32 s64, s64, s50
	s_add_u32 s36, s6, s64
	s_addc_u32 s37, s7, 0
	s_lshl_b32 s64, s33, 3
	s_add_u32 s64, s64, s29
	s_lshl_b32 s64, s64, 5
	s_add_u32 s64, s64, s30
	s_lshl_b32 s64, s64, 2
	s_add_u32 s40, s8, s64
	s_addc_u32 s41, s9, 0
	s_lshl_b32 s64, s33, 19
	s_add_u32 s72, s62, s64
	s_addc_u32 s73, s63, 0
	s_waitcnt vmcnt(9)
	s_barrier
	s_waitcnt lgkmcnt(4)
	v_mfma_f32_32x32x16_f16 v[0:15], a[240:243], v[160:163], v[0:15]
	ds_read_b128 v[160:163], v192 offset:0
	v_mfma_f32_32x32x16_f16 v[16:31], a[240:243], v[164:167], v[16:31]
	ds_read_b128 v[164:167], v192 offset:1024
	v_mfma_f32_32x32x16_f16 v[0:15], a[244:247], v[168:171], v[0:15]
	ds_read_b128 v[168:171], v192 offset:2048
	v_mfma_f32_32x32x16_f16 v[16:31], a[244:247], v[172:175], v[16:31]
	ds_read_b128 v[172:175], v192 offset:3072
	global_load_lds_dwordx4 v192, s[44:45] offset:3072 sc1
	s_waitcnt lgkmcnt(4)
	v_mfma_f32_32x32x16_f16 v[0:15], a[248:251], v[176:179], v[0:15]
	ds_read_b128 v[176:179], v192 offset:4096
	v_mfma_f32_32x32x16_f16 v[16:31], a[248:251], v[180:183], v[16:31]
	ds_read_b128 v[180:183], v192 offset:5120
	v_mfma_f32_32x32x16_f16 v[0:15], a[252:255], v[184:187], v[0:15]
	ds_read_b128 v[184:187], v192 offset:6144
	v_mfma_f32_32x32x16_f16 v[16:31], a[252:255], v[188:191], v[16:31]
	ds_read_b128 v[188:191], v192 offset:7168
	s_add_u32 s44, s34, 0x10000
	s_addc_u32 s45, s35, 0
	s_mov_b32 m0, s56
	s_nop 0
	global_load_lds_dwordx4 v192, s[44:45] sc1
	s_nop 3
	s_waitcnt lgkmcnt(4)
	v_mfma_f32_32x32x16_f16 v[32:47], a[0:3], v[160:163], v[32:47]
	ds_read_b128 v[160:163], v192 offset:8192
	v_exp_f32_e32 v200, v0
	v_mfma_f32_32x32x16_f16 v[48:63], a[0:3], v[164:167], v[48:63]
	ds_read_b128 v[164:167], v192 offset:9216
	s_lshl_b32 s64, s71, 3
	s_add_u32 s64, s64, s29
	s_lshl_b32 s64, s64, 7
	s_add_u32 s38, s8, s64
	s_addc_u32 s39, s9, 0
	global_load_dword v251, v196, s[38:39] sc1
	v_exp_f32_e32 v201, v1
	v_add_f32_e32 v200, 1.0, v200
	v_mfma_f32_32x32x16_f16 v[32:47], a[4:7], v[168:171], v[32:47]
	ds_read_b128 v[168:171], v192 offset:10240
	v_exp_f32_e32 v202, v2
	v_add_f32_e32 v201, 1.0, v201
	v_mfma_f32_32x32x16_f16 v[48:63], a[4:7], v[172:175], v[48:63]
	ds_read_b128 v[172:175], v192 offset:11264
	global_load_lds_dwordx4 v192, s[44:45] offset:1024 sc1
	v_exp_f32_e32 v203, v3
	v_add_f32_e32 v202, 1.0, v202
	s_waitcnt lgkmcnt(4)
	v_mfma_f32_32x32x16_f16 v[32:47], a[8:11], v[176:179], v[32:47]
	ds_read_b128 v[176:179], v192 offset:12288
	v_exp_f32_e32 v204, v4
	v_add_f32_e32 v203, 1.0, v203
	v_mfma_f32_32x32x16_f16 v[48:63], a[8:11], v[180:183], v[48:63]
	ds_read_b128 v[180:183], v192 offset:13312
	v_exp_f32_e32 v205, v5
	v_add_f32_e32 v204, 1.0, v204
	v_mfma_f32_32x32x16_f16 v[32:47], a[12:15], v[184:187], v[32:47]
	ds_read_b128 v[184:187], v192 offset:14336
	v_exp_f32_e32 v206, v6
	v_add_f32_e32 v205, 1.0, v205
	v_mfma_f32_32x32x16_f16 v[48:63], a[12:15], v[188:191], v[48:63]
	ds_read_b128 v[188:191], v192 offset:15360
	global_load_lds_dwordx4 v192, s[44:45] offset:2048 sc1
	v_exp_f32_e32 v207, v7
	v_add_f32_e32 v206, 1.0, v206
	s_waitcnt lgkmcnt(4)
	v_mfma_f32_32x32x16_f16 v[32:47], a[16:19], v[160:163], v[32:47]
	ds_read_b128 v[160:163], v192 offset:16384
	v_exp_f32_e32 v208, v8
	v_add_f32_e32 v207, 1.0, v207
	v_mfma_f32_32x32x16_f16 v[48:63], a[16:19], v[164:167], v[48:63]
	ds_read_b128 v[164:167], v192 offset:17408
	v_exp_f32_e32 v209, v9
	v_add_f32_e32 v208, 1.0, v208
	v_mfma_f32_32x32x16_f16 v[32:47], a[20:23], v[168:171], v[32:47]
	ds_read_b128 v[168:171], v192 offset:18432
	v_exp_f32_e32 v210, v10
	v_add_f32_e32 v209, 1.0, v209
	v_mfma_f32_32x32x16_f16 v[48:63], a[20:23], v[172:175], v[48:63]
	ds_read_b128 v[172:175], v192 offset:19456
	global_load_lds_dwordx4 v192, s[44:45] offset:3072 sc1
	v_exp_f32_e32 v211, v11
	v_add_f32_e32 v210, 1.0, v210
	s_waitcnt lgkmcnt(4)
	v_mfma_f32_32x32x16_f16 v[32:47], a[24:27], v[176:179], v[32:47]
	ds_read_b128 v[176:179], v192 offset:20480
	v_exp_f32_e32 v212, v12
	v_add_f32_e32 v211, 1.0, v211
	v_mfma_f32_32x32x16_f16 v[48:63], a[24:27], v[180:183], v[48:63]
	ds_read_b128 v[180:183], v192 offset:21504
	v_exp_f32_e32 v213, v13
	v_add_f32_e32 v212, 1.0, v212
	v_mfma_f32_32x32x16_f16 v[32:47], a[28:31], v[184:187], v[32:47]
	ds_read_b128 v[184:187], v192 offset:22528
	v_exp_f32_e32 v214, v14
	v_add_f32_e32 v213, 1.0, v213
	v_mfma_f32_32x32x16_f16 v[48:63], a[28:31], v[188:191], v[48:63]
	ds_read_b128 v[188:191], v192 offset:23552
	s_add_u32 s44, s34, 0x11000
	s_addc_u32 s45, s35, 0
	s_mov_b32 m0, s57
	s_nop 0
	global_load_lds_dwordx4 v192, s[44:45] sc1
	v_exp_f32_e32 v215, v15
	v_add_f32_e32 v214, 1.0, v214
	s_waitcnt lgkmcnt(4)
	v_mfma_f32_32x32x16_f16 v[32:47], a[32:35], v[160:163], v[32:47]
	ds_read_b128 v[160:163], v192 offset:24576
	v_add_f32_e32 v215, 1.0, v215
	v_rcp_f32_e32 v200, v200
	v_mfma_f32_32x32x16_f16 v[48:63], a[32:35], v[164:167], v[48:63]
	ds_read_b128 v[164:167], v192 offset:25600
	v_rcp_f32_e32 v201, v201
	v_mfma_f32_32x32x16_f16 v[32:47], a[36:39], v[168:171], v[32:47]
	ds_read_b128 v[168:171], v192 offset:26624
	v_rcp_f32_e32 v202, v202
	v_mfma_f32_32x32x16_f16 v[48:63], a[36:39], v[172:175], v[48:63]
	ds_read_b128 v[172:175], v192 offset:27648
	global_load_lds_dwordx4 v192, s[44:45] offset:1024 sc1
	v_rcp_f32_e32 v203, v203
	s_waitcnt lgkmcnt(4)
	v_mfma_f32_32x32x16_f16 v[32:47], a[40:43], v[176:179], v[32:47]
	ds_read_b128 v[176:179], v192 offset:28672
	v_rcp_f32_e32 v204, v204
	v_mfma_f32_32x32x16_f16 v[48:63], a[40:43], v[180:183], v[48:63]
	ds_read_b128 v[180:183], v192 offset:29696
	v_rcp_f32_e32 v205, v205
	v_mul_f32_e32 v204, v204, v128
	v_mfma_f32_32x32x16_f16 v[32:47], a[44:47], v[184:187], v[32:47]
	ds_read_b128 v[184:187], v192 offset:30720
	v_rcp_f32_e32 v206, v206
	v_mul_f32_e32 v205, v205, v129
	v_mfma_f32_32x32x16_f16 v[48:63], a[44:47], v[188:191], v[48:63]
	ds_read_b128 v[188:191], v192 offset:31744
	global_load_lds_dwordx4 v192, s[44:45] offset:2048 sc1
	v_rcp_f32_e32 v207, v207
	v_mul_f32_e32 v206, v206, v130
	s_waitcnt vmcnt(8)
	s_barrier
	s_waitcnt lgkmcnt(4)
	v_mfma_f32_32x32x16_f16 v[32:47], a[48:51], v[160:163], v[32:47]
	ds_read_b128 v[160:163], v192 offset:32768
	v_rcp_f32_e32 v208, v208
	v_mul_f32_e32 v207, v207, v131
	v_mfma_f32_32x32x16_f16 v[48:63], a[48:51], v[164:167], v[48:63]
	ds_read_b128 v[164:167], v192 offset:33792
	v_rcp_f32_e32 v209, v209
	v_fmamk_f32 v208, v208, 0xc0b8aa3b, v198
	v_mfma_f32_32x32x16_f16 v[32:47], a[52:55], v[168:171], v[32:47]
	ds_read_b128 v[168:171], v192 offset:34816
	v_rcp_f32_e32 v210, v210
	v_fmamk_f32 v209, v209, 0xc0b8aa3b, v198
	v_fma_f32 v128, v200, v208, v204
	v_mfma_f32_32x32x16_f16 v[48:63], a[52:55], v[172:175], v[48:63]
	ds_read_b128 v[172:175], v192 offset:35840
	global_load_lds_dwordx4 v192, s[44:45] offset:3072 sc1
	v_rcp_f32_e32 v211, v211
	v_fmamk_f32 v210, v210, 0xc0b8aa3b, v198
	v_fma_f32 v129, v201, v209, v205
	s_waitcnt lgkmcnt(4)
	v_mfma_f32_32x32x16_f16 v[32:47], a[56:59], v[176:179], v[32:47]
	ds_read_b128 v[176:179], v192 offset:36864
	v_rcp_f32_e32 v212, v212
	v_fmamk_f32 v211, v211, 0xc0b8aa3b, v198
	v_fma_f32 v130, v202, v210, v206
	v_mfma_f32_32x32x16_f16 v[48:63], a[56:59], v[180:183], v[48:63]
	ds_read_b128 v[180:183], v192 offset:37888
	v_rcp_f32_e32 v213, v213
	v_fma_f32 v131, v203, v211, v207
	v_mfma_f32_32x32x16_f16 v[32:47], a[60:63], v[184:187], v[32:47]
	ds_read_b128 v[184:187], v192 offset:38912
	v_rcp_f32_e32 v214, v214
	v_mfma_f32_32x32x16_f16 v[48:63], a[60:63], v[188:191], v[48:63]
	ds_read_b128 v[188:191], v192 offset:39936
	s_add_u32 s44, s34, 0x18000
	s_addc_u32 s45, s35, 0
	s_mov_b32 m0, s58
	s_nop 0
	global_load_lds_dwordx4 v192, s[44:45] sc1
	v_rcp_f32_e32 v215, v215
	s_waitcnt lgkmcnt(4)
	v_mfma_f32_32x32x16_f16 v[32:47], a[64:67], v[160:163], v[32:47]
	ds_read_b128 v[160:163], v192 offset:40960
	v_exp_f32_e32 v200, v128
	v_mfma_f32_32x32x16_f16 v[48:63], a[64:67], v[164:167], v[48:63]
	ds_read_b128 v[164:167], v192 offset:41984
	v_exp_f32_e32 v201, v129
	v_add_f32_e32 v200, 1.0, v200
	v_mfma_f32_32x32x16_f16 v[32:47], a[68:71], v[168:171], v[32:47]
	ds_read_b128 v[168:171], v192 offset:43008
	v_exp_f32_e32 v202, v130
	v_add_f32_e32 v201, 1.0, v201
	v_mfma_f32_32x32x16_f16 v[48:63], a[68:71], v[172:175], v[48:63]
	ds_read_b128 v[172:175], v192 offset:44032
	global_load_lds_dwordx4 v192, s[44:45] offset:1024 sc1
	v_exp_f32_e32 v203, v131
	v_add_f32_e32 v202, 1.0, v202
	s_waitcnt lgkmcnt(4)
	v_mfma_f32_32x32x16_f16 v[32:47], a[72:75], v[176:179], v[32:47]
	ds_read_b128 v[176:179], v192 offset:45056
	v_add_f32_e32 v203, 1.0, v203
	v_rcp_f32_e32 v200, v200
	v_mfma_f32_32x32x16_f16 v[48:63], a[72:75], v[180:183], v[48:63]
	ds_read_b128 v[180:183], v192 offset:46080
	v_rcp_f32_e32 v201, v201
	v_fma_f32 v200, v200, 2.0, -1.0
	v_mfma_f32_32x32x16_f16 v[32:47], a[76:79], v[184:187], v[32:47]
	ds_read_b128 v[184:187], v192 offset:47104
	v_rcp_f32_e32 v202, v202
	v_fma_f32 v201, v201, 2.0, -1.0
	v_mul_f32_e32 v216, v212, v200
	v_mfma_f32_32x32x16_f16 v[48:63], a[76:79], v[188:191], v[48:63]
	ds_read_b128 v[188:191], v192 offset:48128
	global_load_lds_dwordx4 v192, s[44:45] offset:2048 sc1
	v_rcp_f32_e32 v203, v203
	v_fma_f32 v202, v202, 2.0, -1.0
	v_mul_f32_e32 v217, v213, v201
	s_waitcnt lgkmcnt(4)
	v_mfma_f32_32x32x16_f16 v[32:47], a[80:83], v[160:163], v[32:47]
	ds_read_b128 v[160:163], v192 offset:49152
	v_fma_f32 v203, v203, 2.0, -1.0
	v_mul_f32_e32 v218, v214, v202
	v_exp_f32_e32 v200, v16
	v_mfma_f32_32x32x16_f16 v[48:63], a[80:83], v[164:167], v[48:63]
	ds_read_b128 v[164:167], v192 offset:50176
	v_mul_f32_e32 v219, v215, v203
	v_mul_f32_e32 v236, v216, v228
	v_exp_f32_e32 v201, v17
	v_mfma_f32_32x32x16_f16 v[32:47], a[84:87], v[168:171], v[32:47]
	ds_read_b128 v[168:171], v192 offset:51200
	v_mul_f32_e32 v237, v216, v232
	v_fmac_f32_e32 v236, v217, v229
	v_exp_f32_e32 v202, v18
	v_mfma_f32_32x32x16_f16 v[48:63], a[84:87], v[172:175], v[48:63]
	ds_read_b128 v[172:175], v192 offset:52224
	global_load_lds_dwordx4 v192, s[44:45] offset:3072 sc1
	v_fmac_f32_e32 v237, v217, v233
	v_fmac_f32_e32 v236, v218, v230
	v_exp_f32_e32 v203, v19
	s_waitcnt lgkmcnt(4)
	v_mfma_f32_32x32x16_f16 v[32:47], a[88:91], v[176:179], v[32:47]
	ds_read_b128 v[176:179], v192 offset:53248
	v_fmac_f32_e32 v237, v218, v234
	v_fmac_f32_e32 v236, v219, v231
	v_exp_f32_e32 v204, v20
	v_mfma_f32_32x32x16_f16 v[48:63], a[88:91], v[180:183], v[48:63]
	ds_read_b128 v[180:183], v192 offset:54272
	v_fmac_f32_e32 v237, v219, v235
	v_mov_b32_e32 v238, v236
	v_exp_f32_e32 v205, v21
	v_mfma_f32_32x32x16_f16 v[32:47], a[92:95], v[184:187], v[32:47]
	ds_read_b128 v[184:187], v192 offset:55296
	v_mov_b32_e32 v239, v236
	v_mov_b32_e32 v240, v237
	v_exp_f32_e32 v206, v22
	v_mfma_f32_32x32x16_f16 v[48:63], a[92:95], v[188:191], v[48:63]
	ds_read_b128 v[188:191], v192 offset:56320
	s_add_u32 s44, s34, 0x19000
	s_addc_u32 s45, s35, 0
	s_mov_b32 m0, s59
	s_nop 0
	global_load_lds_dwordx4 v192, s[44:45] sc1
	v_mov_b32_e32 v241, v237
	v_cvt_pk_f16_f32 v220, v216, v217
	v_exp_f32_e32 v207, v23
	s_waitcnt lgkmcnt(4)
	v_mfma_f32_32x32x16_f16 v[32:47], a[96:99], v[160:163], v[32:47]
	ds_read_b128 v[160:163], v192 offset:57344
	s_nop 1
	v_permlane32_swap_b32_e32 v238, v239
	v_permlane32_swap_b32_e32 v240, v241
	v_add_f32_e32 v238, v238, v239
	v_add_f32_e32 v239, v240, v241
	ds_write_b64 v248, v[238:239] offset:0
	v_exp_f32_e32 v208, v24
	v_mfma_f32_32x32x16_f16 v[48:63], a[96:99], v[164:167], v[48:63]
	ds_read_b128 v[164:167], v192 offset:58368
	v_cvt_pk_f16_f32 v221, v218, v219
	v_exp_f32_e32 v209, v25
	v_add_f32_e32 v200, 1.0, v200
	v_mfma_f32_32x32x16_f16 v[32:47], a[100:103], v[168:171], v[32:47]
	ds_read_b128 v[168:171], v192 offset:59392
	v_exp_f32_e32 v210, v26
	v_add_f32_e32 v201, 1.0, v201
	v_add_f32_e32 v202, 1.0, v202
	v_mfma_f32_32x32x16_f16 v[48:63], a[100:103], v[172:175], v[48:63]
	ds_read_b128 v[172:175], v192 offset:60416
	global_load_lds_dwordx4 v192, s[44:45] offset:1024 sc1
	v_exp_f32_e32 v211, v27
	v_add_f32_e32 v203, 1.0, v203
	v_add_f32_e32 v204, 1.0, v204
	s_waitcnt lgkmcnt(5)
	v_mfma_f32_32x32x16_f16 v[32:47], a[104:107], v[176:179], v[32:47]
	ds_read_b128 v[176:179], v192 offset:61440
	v_exp_f32_e32 v212, v28
	v_add_f32_e32 v205, 1.0, v205
	v_add_f32_e32 v206, 1.0, v206
	v_mfma_f32_32x32x16_f16 v[48:63], a[104:107], v[180:183], v[48:63]
	ds_read_b128 v[180:183], v192 offset:62464
	v_exp_f32_e32 v213, v29
	v_add_f32_e32 v207, 1.0, v207
	v_add_f32_e32 v208, 1.0, v208
	v_mfma_f32_32x32x16_f16 v[32:47], a[108:111], v[184:187], v[32:47]
	ds_read_b128 v[184:187], v192 offset:63488
	v_exp_f32_e32 v214, v30
	v_add_f32_e32 v209, 1.0, v209
	v_add_f32_e32 v210, 1.0, v210
	v_mfma_f32_32x32x16_f16 v[48:63], a[108:111], v[188:191], v[48:63]
	ds_read_b128 v[188:191], v192 offset:64512
	global_load_lds_dwordx4 v192, s[44:45] offset:2048 sc1
	v_exp_f32_e32 v215, v31
	v_add_f32_e32 v211, 1.0, v211
	v_add_f32_e32 v212, 1.0, v212
	s_waitcnt vmcnt(7)
	s_barrier
	s_waitcnt lgkmcnt(4)
	v_mfma_f32_32x32x16_f16 v[32:47], a[112:115], v[160:163], v[32:47]
	ds_read_b128 v[160:163], v193 offset:0
	v_add_f32_e32 v213, 1.0, v213
	v_add_f32_e32 v214, 1.0, v214
	v_rcp_f32_e32 v200, v200
	v_mfma_f32_32x32x16_f16 v[48:63], a[112:115], v[164:167], v[48:63]
	ds_read_b128 v[164:167], v193 offset:1024
	v_add_f32_e32 v215, 1.0, v215
	v_rcp_f32_e32 v201, v201
	v_mfma_f32_32x32x16_f16 v[32:47], a[116:119], v[168:171], v[32:47]
	ds_read_b128 v[168:171], v193 offset:2048
	v_rcp_f32_e32 v202, v202
	v_mfma_f32_32x32x16_f16 v[48:63], a[116:119], v[172:175], v[48:63]
	ds_read_b128 v[172:175], v193 offset:3072
	global_load_lds_dwordx4 v192, s[44:45] offset:3072 sc1
	v_rcp_f32_e32 v203, v203
	s_waitcnt lgkmcnt(4)
	v_mfma_f32_32x32x16_f16 v[32:47], a[120:123], v[176:179], v[32:47]
	ds_read_b128 v[176:179], v193 offset:4096
	v_rcp_f32_e32 v204, v204
	s_add_u32 s46, s42, 0x6000
	s_addc_u32 s47, s43, 0
	global_load_dwordx4 v[96:99], v192, s[46:47] offset:0
	v_mfma_f32_32x32x16_f16 v[48:63], a[120:123], v[180:183], v[48:63]
	ds_read_b128 v[180:183], v193 offset:5120
	v_rcp_f32_e32 v205, v205
	v_mul_f32_e32 v204, v204, v132
	global_load_dwordx4 v[100:103], v192, s[46:47] offset:1024
	global_load_dwordx4 v[104:107], v192, s[46:47] offset:2048
	v_mfma_f32_32x32x16_f16 v[32:47], a[124:127], v[184:187], v[32:47]
	ds_read_b128 v[184:187], v193 offset:6144
	v_rcp_f32_e32 v206, v206
	v_mul_f32_e32 v205, v205, v133
	global_load_dwordx4 v[108:111], v192, s[46:47] offset:3072
	s_add_u32 s46, s42, 0x7000
	s_addc_u32 s47, s43, 0
	v_mfma_f32_32x32x16_f16 v[48:63], a[124:127], v[188:191], v[48:63]
	ds_read_b128 v[188:191], v193 offset:7168
	v_cmp_gt_u32_e32 vcc, 3, v251
	s_cbranch_vccz .LD_tok26

.LD_join31:
	ds_read_b64 v[200:201], v249 offset:0
	ds_read_b64 v[202:203], v249 offset:2048
	ds_read_b64 v[204:205], v249 offset:4096
	ds_read_b64 v[206:207], v249 offset:6144
	s_waitcnt lgkmcnt(8)
	v_mfma_f32_32x32x16_f16 v[32:47], a[208:211], v[160:163], v[32:47]
	ds_read_b128 v[160:163], v193 offset:49152
	v_mfma_f32_32x32x16_f16 v[48:63], a[208:211], v[164:167], v[48:63]
	ds_read_b128 v[164:167], v193 offset:50176
	v_mfma_f32_32x32x16_f16 v[32:47], a[212:215], v[168:171], v[32:47]
	ds_read_b128 v[168:171], v193 offset:51200
	v_mfma_f32_32x32x16_f16 v[48:63], a[212:215], v[172:175], v[48:63]
	ds_read_b128 v[172:175], v193 offset:52224
	global_load_lds_dwordx4 v192, s[44:45] offset:3072 sc1
	s_waitcnt lgkmcnt(8)
	v_mfma_f32_32x32x16_f16 v[32:47], a[216:219], v[176:179], v[32:47]
	ds_read_b128 v[176:179], v193 offset:53248
	v_mfma_f32_32x32x16_f16 v[48:63], a[216:219], v[180:183], v[48:63]
	ds_read_b128 v[180:183], v193 offset:54272
	v_mfma_f32_32x32x16_f16 v[32:47], a[220:223], v[184:187], v[32:47]
	ds_read_b128 v[184:187], v193 offset:55296
	v_mfma_f32_32x32x16_f16 v[48:63], a[220:223], v[188:191], v[48:63]
	ds_read_b128 v[188:191], v193 offset:56320
	s_add_u32 s44, s34, 0x9000
	s_addc_u32 s45, s35, 0
	s_mov_b32 m0, s55
	s_nop 0
	global_load_lds_dwordx4 v192, s[44:45] sc1
	s_waitcnt lgkmcnt(4)
	v_mfma_f32_32x32x16_f16 v[32:47], a[224:227], v[160:163], v[32:47]
	ds_read_b128 v[160:163], v193 offset:57344
	v_mfma_f32_32x32x16_f16 v[48:63], a[224:227], v[164:167], v[48:63]
	ds_read_b128 v[164:167], v193 offset:58368
	v_mfma_f32_32x32x16_f16 v[32:47], a[228:231], v[168:171], v[32:47]
	ds_read_b128 v[168:171], v193 offset:59392
	v_mfma_f32_32x32x16_f16 v[48:63], a[228:231], v[172:175], v[48:63]
	ds_read_b128 v[172:175], v193 offset:60416
	global_load_lds_dwordx4 v192, s[44:45] offset:1024 sc1
	v_add_f32_e32 v200, v200, v202
	v_add_f32_e32 v201, v201, v203
	v_add_f32_e32 v200, v200, v204
	v_add_f32_e32 v201, v201, v205
	v_add_f32_e32 v200, v200, v206
	v_add_f32_e32 v201, v201, v207
	global_store_dwordx2 v250, v[200:201], s[72:73]
	s_waitcnt lgkmcnt(4)
	v_mfma_f32_32x32x16_f16 v[32:47], a[232:235], v[176:179], v[32:47]
	ds_read_b128 v[176:179], v193 offset:61440
	v_mfma_f32_32x32x16_f16 v[48:63], a[232:235], v[180:183], v[48:63]
	ds_read_b128 v[180:183], v193 offset:62464
	v_mfma_f32_32x32x16_f16 v[32:47], a[236:239], v[184:187], v[32:47]
	ds_read_b128 v[184:187], v193 offset:63488
	v_mfma_f32_32x32x16_f16 v[48:63], a[236:239], v[188:191], v[48:63]
	ds_read_b128 v[188:191], v193 offset:64512
	global_load_lds_dwordx4 v192, s[44:45] offset:2048 sc1
	s_and_b32 s64, s33, 1
	s_lshl_b32 s64, s64, 22
	s_add_u32 s64, s64, s50
	s_add_u32 s64, s64, 0x20000
	s_add_u32 s36, s6, s64
	s_addc_u32 s37, s7, 0
	s_lshl_b32 s64, s33, 3
	s_add_u32 s64, s64, s29
	s_lshl_b32 s64, s64, 5
	s_add_u32 s64, s64, s30
	s_lshl_b32 s64, s64, 2
	s_add_u32 s40, s8, s64
	s_addc_u32 s41, s9, 0
	s_lshl_b32 s64, s33, 19
	s_add_u32 s64, s64, 0x200
	s_add_u32 s72, s62, s64
	s_addc_u32 s73, s63, 0
	s_waitcnt vmcnt(9)
	s_barrier
	s_waitcnt lgkmcnt(4)
	v_mfma_f32_32x32x16_f16 v[32:47], a[240:243], v[160:163], v[32:47]
	ds_read_b128 v[160:163], v192 offset:0
	v_mfma_f32_32x32x16_f16 v[48:63], a[240:243], v[164:167], v[48:63]
	ds_read_b128 v[164:167], v192 offset:1024
	v_mfma_f32_32x32x16_f16 v[32:47], a[244:247], v[168:171], v[32:47]
	ds_read_b128 v[168:171], v192 offset:2048
	v_mfma_f32_32x32x16_f16 v[48:63], a[244:247], v[172:175], v[48:63]
	ds_read_b128 v[172:175], v192 offset:3072
	global_load_lds_dwordx4 v192, s[44:45] offset:3072 sc1
	s_waitcnt lgkmcnt(4)
	v_mfma_f32_32x32x16_f16 v[32:47], a[248:251], v[176:179], v[32:47]
	ds_read_b128 v[176:179], v192 offset:4096
	v_mfma_f32_32x32x16_f16 v[48:63], a[248:251], v[180:183], v[48:63]
	ds_read_b128 v[180:183], v192 offset:5120
	v_mfma_f32_32x32x16_f16 v[32:47], a[252:255], v[184:187], v[32:47]
	ds_read_b128 v[184:187], v192 offset:6144
	v_mfma_f32_32x32x16_f16 v[48:63], a[252:255], v[188:191], v[48:63]
	ds_read_b128 v[188:191], v192 offset:7168
	s_add_u32 s44, s34, 0x10000
	s_addc_u32 s45, s35, 0
	s_mov_b32 m0, s56
	s_nop 0
	global_load_lds_dwordx4 v192, s[44:45] sc1
	s_nop 3
	s_waitcnt lgkmcnt(4)
	v_mfma_f32_32x32x16_f16 v[64:79], a[0:3], v[160:163], v[64:79]
	ds_read_b128 v[160:163], v192 offset:8192
	v_exp_f32_e32 v200, v32
	v_mfma_f32_32x32x16_f16 v[80:95], a[0:3], v[164:167], v[80:95]
	ds_read_b128 v[164:167], v192 offset:9216
	s_lshl_b32 s64, s71, 3
	s_add_u32 s64, s64, s29
	s_lshl_b32 s64, s64, 7
	s_add_u32 s38, s8, s64
	s_addc_u32 s39, s9, 0
	global_load_dword v251, v196, s[38:39] sc1
	v_exp_f32_e32 v201, v33
	v_add_f32_e32 v200, 1.0, v200
	v_mfma_f32_32x32x16_f16 v[64:79], a[4:7], v[168:171], v[64:79]
	ds_read_b128 v[168:171], v192 offset:10240
	v_exp_f32_e32 v202, v34
	v_add_f32_e32 v201, 1.0, v201
	v_mfma_f32_32x32x16_f16 v[80:95], a[4:7], v[172:175], v[80:95]
	ds_read_b128 v[172:175], v192 offset:11264
	global_load_lds_dwordx4 v192, s[44:45] offset:1024 sc1
	v_exp_f32_e32 v203, v35
	v_add_f32_e32 v202, 1.0, v202
	s_waitcnt lgkmcnt(4)
	v_mfma_f32_32x32x16_f16 v[64:79], a[8:11], v[176:179], v[64:79]
	ds_read_b128 v[176:179], v192 offset:12288
	v_exp_f32_e32 v204, v36
	v_add_f32_e32 v203, 1.0, v203
	v_mfma_f32_32x32x16_f16 v[80:95], a[8:11], v[180:183], v[80:95]
	ds_read_b128 v[180:183], v192 offset:13312
	v_exp_f32_e32 v205, v37
	v_add_f32_e32 v204, 1.0, v204
	v_mfma_f32_32x32x16_f16 v[64:79], a[12:15], v[184:187], v[64:79]
	ds_read_b128 v[184:187], v192 offset:14336
	v_exp_f32_e32 v206, v38
	v_add_f32_e32 v205, 1.0, v205
	v_mfma_f32_32x32x16_f16 v[80:95], a[12:15], v[188:191], v[80:95]
	ds_read_b128 v[188:191], v192 offset:15360
	global_load_lds_dwordx4 v192, s[44:45] offset:2048 sc1
	v_exp_f32_e32 v207, v39
	v_add_f32_e32 v206, 1.0, v206
	s_waitcnt lgkmcnt(4)
	v_mfma_f32_32x32x16_f16 v[64:79], a[16:19], v[160:163], v[64:79]
	ds_read_b128 v[160:163], v192 offset:16384
	v_exp_f32_e32 v208, v40
	v_add_f32_e32 v207, 1.0, v207
	v_mfma_f32_32x32x16_f16 v[80:95], a[16:19], v[164:167], v[80:95]
	ds_read_b128 v[164:167], v192 offset:17408
	v_exp_f32_e32 v209, v41
	v_add_f32_e32 v208, 1.0, v208
	v_mfma_f32_32x32x16_f16 v[64:79], a[20:23], v[168:171], v[64:79]
	ds_read_b128 v[168:171], v192 offset:18432
	v_exp_f32_e32 v210, v42
	v_add_f32_e32 v209, 1.0, v209
	v_mfma_f32_32x32x16_f16 v[80:95], a[20:23], v[172:175], v[80:95]
	ds_read_b128 v[172:175], v192 offset:19456
	global_load_lds_dwordx4 v192, s[44:45] offset:3072 sc1
	v_exp_f32_e32 v211, v43
	v_add_f32_e32 v210, 1.0, v210
	s_waitcnt lgkmcnt(4)
	v_mfma_f32_32x32x16_f16 v[64:79], a[24:27], v[176:179], v[64:79]
	ds_read_b128 v[176:179], v192 offset:20480
	v_exp_f32_e32 v212, v44
	v_add_f32_e32 v211, 1.0, v211
	v_mfma_f32_32x32x16_f16 v[80:95], a[24:27], v[180:183], v[80:95]
	ds_read_b128 v[180:183], v192 offset:21504
	v_exp_f32_e32 v213, v45
	v_add_f32_e32 v212, 1.0, v212
	v_mfma_f32_32x32x16_f16 v[64:79], a[28:31], v[184:187], v[64:79]
	ds_read_b128 v[184:187], v192 offset:22528
	v_exp_f32_e32 v214, v46
	v_add_f32_e32 v213, 1.0, v213
	v_mfma_f32_32x32x16_f16 v[80:95], a[28:31], v[188:191], v[80:95]
	ds_read_b128 v[188:191], v192 offset:23552
	s_add_u32 s44, s34, 0x11000
	s_addc_u32 s45, s35, 0
	s_mov_b32 m0, s57
	s_nop 0
	global_load_lds_dwordx4 v192, s[44:45] sc1
	v_exp_f32_e32 v215, v47
	v_add_f32_e32 v214, 1.0, v214
	s_waitcnt lgkmcnt(4)
	v_mfma_f32_32x32x16_f16 v[64:79], a[32:35], v[160:163], v[64:79]
	ds_read_b128 v[160:163], v192 offset:24576
	v_add_f32_e32 v215, 1.0, v215
	v_rcp_f32_e32 v200, v200
	v_mfma_f32_32x32x16_f16 v[80:95], a[32:35], v[164:167], v[80:95]
	ds_read_b128 v[164:167], v192 offset:25600
	v_rcp_f32_e32 v201, v201
	v_mfma_f32_32x32x16_f16 v[64:79], a[36:39], v[168:171], v[64:79]
	ds_read_b128 v[168:171], v192 offset:26624
	v_rcp_f32_e32 v202, v202
	v_mfma_f32_32x32x16_f16 v[80:95], a[36:39], v[172:175], v[80:95]
	ds_read_b128 v[172:175], v192 offset:27648
	global_load_lds_dwordx4 v192, s[44:45] offset:1024 sc1
	v_rcp_f32_e32 v203, v203
	s_waitcnt lgkmcnt(4)
	v_mfma_f32_32x32x16_f16 v[64:79], a[40:43], v[176:179], v[64:79]
	ds_read_b128 v[176:179], v192 offset:28672
	v_rcp_f32_e32 v204, v204
	v_mfma_f32_32x32x16_f16 v[80:95], a[40:43], v[180:183], v[80:95]
	ds_read_b128 v[180:183], v192 offset:29696
	v_rcp_f32_e32 v205, v205
	v_mul_f32_e32 v204, v204, v136
	v_mfma_f32_32x32x16_f16 v[64:79], a[44:47], v[184:187], v[64:79]
	ds_read_b128 v[184:187], v192 offset:30720
	v_rcp_f32_e32 v206, v206
	v_mul_f32_e32 v205, v205, v137
	v_mfma_f32_32x32x16_f16 v[80:95], a[44:47], v[188:191], v[80:95]
	ds_read_b128 v[188:191], v192 offset:31744
	global_load_lds_dwordx4 v192, s[44:45] offset:2048 sc1
	v_rcp_f32_e32 v207, v207
	v_mul_f32_e32 v206, v206, v138
	s_waitcnt vmcnt(8)
	s_barrier
	s_waitcnt lgkmcnt(4)
	v_mfma_f32_32x32x16_f16 v[64:79], a[48:51], v[160:163], v[64:79]
	ds_read_b128 v[160:163], v192 offset:32768
	v_rcp_f32_e32 v208, v208
	v_mul_f32_e32 v207, v207, v139
	v_mfma_f32_32x32x16_f16 v[80:95], a[48:51], v[164:167], v[80:95]
	ds_read_b128 v[164:167], v192 offset:33792
	v_rcp_f32_e32 v209, v209
	v_fmamk_f32 v208, v208, 0xc0b8aa3b, v198
	v_mfma_f32_32x32x16_f16 v[64:79], a[52:55], v[168:171], v[64:79]
	ds_read_b128 v[168:171], v192 offset:34816
	v_rcp_f32_e32 v210, v210
	v_fmamk_f32 v209, v209, 0xc0b8aa3b, v198
	v_fma_f32 v136, v200, v208, v204
	v_mfma_f32_32x32x16_f16 v[80:95], a[52:55], v[172:175], v[80:95]
	ds_read_b128 v[172:175], v192 offset:35840
	global_load_lds_dwordx4 v192, s[44:45] offset:3072 sc1
	v_rcp_f32_e32 v211, v211
	v_fmamk_f32 v210, v210, 0xc0b8aa3b, v198
	v_fma_f32 v137, v201, v209, v205
	s_waitcnt lgkmcnt(4)
	v_mfma_f32_32x32x16_f16 v[64:79], a[56:59], v[176:179], v[64:79]
	ds_read_b128 v[176:179], v192 offset:36864
	v_rcp_f32_e32 v212, v212
	v_fmamk_f32 v211, v211, 0xc0b8aa3b, v198
	v_fma_f32 v138, v202, v210, v206
	v_mfma_f32_32x32x16_f16 v[80:95], a[56:59], v[180:183], v[80:95]
	ds_read_b128 v[180:183], v192 offset:37888
	v_rcp_f32_e32 v213, v213
	v_fma_f32 v139, v203, v211, v207
	v_mfma_f32_32x32x16_f16 v[64:79], a[60:63], v[184:187], v[64:79]
	ds_read_b128 v[184:187], v192 offset:38912
	v_rcp_f32_e32 v214, v214
	v_mfma_f32_32x32x16_f16 v[80:95], a[60:63], v[188:191], v[80:95]
	ds_read_b128 v[188:191], v192 offset:39936
	s_add_u32 s44, s34, 0x18000
	s_addc_u32 s45, s35, 0
	s_mov_b32 m0, s58
	s_nop 0
	global_load_lds_dwordx4 v192, s[44:45] sc1
	v_rcp_f32_e32 v215, v215
	s_waitcnt lgkmcnt(4)
	v_mfma_f32_32x32x16_f16 v[64:79], a[64:67], v[160:163], v[64:79]
	ds_read_b128 v[160:163], v192 offset:40960
	v_exp_f32_e32 v200, v136
	v_mfma_f32_32x32x16_f16 v[80:95], a[64:67], v[164:167], v[80:95]
	ds_read_b128 v[164:167], v192 offset:41984
	v_exp_f32_e32 v201, v137
	v_add_f32_e32 v200, 1.0, v200
	v_mfma_f32_32x32x16_f16 v[64:79], a[68:71], v[168:171], v[64:79]
	ds_read_b128 v[168:171], v192 offset:43008
	v_exp_f32_e32 v202, v138
	v_add_f32_e32 v201, 1.0, v201
	v_mfma_f32_32x32x16_f16 v[80:95], a[68:71], v[172:175], v[80:95]
	ds_read_b128 v[172:175], v192 offset:44032
	global_load_lds_dwordx4 v192, s[44:45] offset:1024 sc1
	v_exp_f32_e32 v203, v139
	v_add_f32_e32 v202, 1.0, v202
	s_waitcnt lgkmcnt(4)
	v_mfma_f32_32x32x16_f16 v[64:79], a[72:75], v[176:179], v[64:79]
	ds_read_b128 v[176:179], v192 offset:45056
	v_add_f32_e32 v203, 1.0, v203
	v_rcp_f32_e32 v200, v200
	v_mfma_f32_32x32x16_f16 v[80:95], a[72:75], v[180:183], v[80:95]
	ds_read_b128 v[180:183], v192 offset:46080
	v_rcp_f32_e32 v201, v201
	v_fma_f32 v200, v200, 2.0, -1.0
	v_mfma_f32_32x32x16_f16 v[64:79], a[76:79], v[184:187], v[64:79]
	ds_read_b128 v[184:187], v192 offset:47104
	v_rcp_f32_e32 v202, v202
	v_fma_f32 v201, v201, 2.0, -1.0
	v_mul_f32_e32 v216, v212, v200
	v_mfma_f32_32x32x16_f16 v[80:95], a[76:79], v[188:191], v[80:95]
	ds_read_b128 v[188:191], v192 offset:48128
	global_load_lds_dwordx4 v192, s[44:45] offset:2048 sc1
	v_rcp_f32_e32 v203, v203
	v_fma_f32 v202, v202, 2.0, -1.0
	v_mul_f32_e32 v217, v213, v201
	s_waitcnt lgkmcnt(4)
	v_mfma_f32_32x32x16_f16 v[64:79], a[80:83], v[160:163], v[64:79]
	ds_read_b128 v[160:163], v192 offset:49152
	v_fma_f32 v203, v203, 2.0, -1.0
	v_mul_f32_e32 v218, v214, v202
	v_exp_f32_e32 v200, v48
	v_mfma_f32_32x32x16_f16 v[80:95], a[80:83], v[164:167], v[80:95]
	ds_read_b128 v[164:167], v192 offset:50176
	v_mul_f32_e32 v219, v215, v203
	v_mul_f32_e32 v236, v216, v228
	v_exp_f32_e32 v201, v49
	v_mfma_f32_32x32x16_f16 v[64:79], a[84:87], v[168:171], v[64:79]
	ds_read_b128 v[168:171], v192 offset:51200
	v_mul_f32_e32 v237, v216, v232
	v_fmac_f32_e32 v236, v217, v229
	v_exp_f32_e32 v202, v50
	v_mfma_f32_32x32x16_f16 v[80:95], a[84:87], v[172:175], v[80:95]
	ds_read_b128 v[172:175], v192 offset:52224
	global_load_lds_dwordx4 v192, s[44:45] offset:3072 sc1
	v_fmac_f32_e32 v237, v217, v233
	v_fmac_f32_e32 v236, v218, v230
	v_exp_f32_e32 v203, v51
	s_waitcnt lgkmcnt(4)
	v_mfma_f32_32x32x16_f16 v[64:79], a[88:91], v[176:179], v[64:79]
	ds_read_b128 v[176:179], v192 offset:53248
	v_fmac_f32_e32 v237, v218, v234
	v_fmac_f32_e32 v236, v219, v231
	v_exp_f32_e32 v204, v52
	v_mfma_f32_32x32x16_f16 v[80:95], a[88:91], v[180:183], v[80:95]
	ds_read_b128 v[180:183], v192 offset:54272
	v_fmac_f32_e32 v237, v219, v235
	v_mov_b32_e32 v238, v236
	v_exp_f32_e32 v205, v53
	v_mfma_f32_32x32x16_f16 v[64:79], a[92:95], v[184:187], v[64:79]
	ds_read_b128 v[184:187], v192 offset:55296
	v_mov_b32_e32 v239, v236
	v_mov_b32_e32 v240, v237
	v_exp_f32_e32 v206, v54
	v_mfma_f32_32x32x16_f16 v[80:95], a[92:95], v[188:191], v[80:95]
	ds_read_b128 v[188:191], v192 offset:56320
	s_add_u32 s44, s34, 0x19000
	s_addc_u32 s45, s35, 0
	s_mov_b32 m0, s59
	s_nop 0
	global_load_lds_dwordx4 v192, s[44:45] sc1
	v_mov_b32_e32 v241, v237
	v_cvt_pk_f16_f32 v220, v216, v217
	v_exp_f32_e32 v207, v55
	s_waitcnt lgkmcnt(4)
	v_mfma_f32_32x32x16_f16 v[64:79], a[96:99], v[160:163], v[64:79]
	ds_read_b128 v[160:163], v192 offset:57344
	s_nop 1
	v_permlane32_swap_b32_e32 v238, v239
	v_permlane32_swap_b32_e32 v240, v241
	v_add_f32_e32 v238, v238, v239
	v_add_f32_e32 v239, v240, v241
	ds_write_b64 v248, v[238:239] offset:512
	v_exp_f32_e32 v208, v56
	v_mfma_f32_32x32x16_f16 v[80:95], a[96:99], v[164:167], v[80:95]
	ds_read_b128 v[164:167], v192 offset:58368
	v_cvt_pk_f16_f32 v221, v218, v219
	v_exp_f32_e32 v209, v57
	v_add_f32_e32 v200, 1.0, v200
	v_mfma_f32_32x32x16_f16 v[64:79], a[100:103], v[168:171], v[64:79]
	ds_read_b128 v[168:171], v192 offset:59392
	v_exp_f32_e32 v210, v58
	v_add_f32_e32 v201, 1.0, v201
	v_add_f32_e32 v202, 1.0, v202
	v_mfma_f32_32x32x16_f16 v[80:95], a[100:103], v[172:175], v[80:95]
	ds_read_b128 v[172:175], v192 offset:60416
	global_load_lds_dwordx4 v192, s[44:45] offset:1024 sc1
	v_exp_f32_e32 v211, v59
	v_add_f32_e32 v203, 1.0, v203
	v_add_f32_e32 v204, 1.0, v204
	s_waitcnt lgkmcnt(5)
	v_mfma_f32_32x32x16_f16 v[64:79], a[104:107], v[176:179], v[64:79]
	ds_read_b128 v[176:179], v192 offset:61440
	v_exp_f32_e32 v212, v60
	v_add_f32_e32 v205, 1.0, v205
	v_add_f32_e32 v206, 1.0, v206
	v_mfma_f32_32x32x16_f16 v[80:95], a[104:107], v[180:183], v[80:95]
	ds_read_b128 v[180:183], v192 offset:62464
	v_exp_f32_e32 v213, v61
	v_add_f32_e32 v207, 1.0, v207
	v_add_f32_e32 v208, 1.0, v208
	v_mfma_f32_32x32x16_f16 v[64:79], a[108:111], v[184:187], v[64:79]
	ds_read_b128 v[184:187], v192 offset:63488
	v_exp_f32_e32 v214, v62
	v_add_f32_e32 v209, 1.0, v209
	v_add_f32_e32 v210, 1.0, v210
	v_mfma_f32_32x32x16_f16 v[80:95], a[108:111], v[188:191], v[80:95]
	ds_read_b128 v[188:191], v192 offset:64512
	global_load_lds_dwordx4 v192, s[44:45] offset:2048 sc1
	v_exp_f32_e32 v215, v63
	v_add_f32_e32 v211, 1.0, v211
	v_add_f32_e32 v212, 1.0, v212
	s_waitcnt vmcnt(7)
	s_barrier
	s_waitcnt lgkmcnt(4)
	v_mfma_f32_32x32x16_f16 v[64:79], a[112:115], v[160:163], v[64:79]
	ds_read_b128 v[160:163], v193 offset:0
	v_add_f32_e32 v213, 1.0, v213
	v_add_f32_e32 v214, 1.0, v214
	v_rcp_f32_e32 v200, v200
	v_mfma_f32_32x32x16_f16 v[80:95], a[112:115], v[164:167], v[80:95]
	ds_read_b128 v[164:167], v193 offset:1024
	v_add_f32_e32 v215, 1.0, v215
	v_rcp_f32_e32 v201, v201
	v_mfma_f32_32x32x16_f16 v[64:79], a[116:119], v[168:171], v[64:79]
	ds_read_b128 v[168:171], v193 offset:2048
	v_rcp_f32_e32 v202, v202
	v_mfma_f32_32x32x16_f16 v[80:95], a[116:119], v[172:175], v[80:95]
	ds_read_b128 v[172:175], v193 offset:3072
	global_load_lds_dwordx4 v192, s[44:45] offset:3072 sc1
	v_rcp_f32_e32 v203, v203
	s_waitcnt lgkmcnt(4)
	v_mfma_f32_32x32x16_f16 v[64:79], a[120:123], v[176:179], v[64:79]
	ds_read_b128 v[176:179], v193 offset:4096
	v_rcp_f32_e32 v204, v204
	s_add_u32 s46, s42, 0x0
	s_addc_u32 s47, s43, 0
	global_load_dwordx4 v[0:3], v192, s[46:47] offset:0
	v_mfma_f32_32x32x16_f16 v[80:95], a[120:123], v[180:183], v[80:95]
	ds_read_b128 v[180:183], v193 offset:5120
	v_rcp_f32_e32 v205, v205
	v_mul_f32_e32 v204, v204, v140
	global_load_dwordx4 v[4:7], v192, s[46:47] offset:1024
	global_load_dwordx4 v[8:11], v192, s[46:47] offset:2048
	v_mfma_f32_32x32x16_f16 v[64:79], a[124:127], v[184:187], v[64:79]
	ds_read_b128 v[184:187], v193 offset:6144
	v_rcp_f32_e32 v206, v206
	v_mul_f32_e32 v205, v205, v141
	global_load_dwordx4 v[12:15], v192, s[46:47] offset:3072
	s_add_u32 s46, s42, 0x1000
	s_addc_u32 s47, s43, 0
	v_mfma_f32_32x32x16_f16 v[80:95], a[124:127], v[188:191], v[80:95]
	ds_read_b128 v[188:191], v193 offset:7168
	v_cmp_gt_u32_e32 vcc, 4, v251
	s_cbranch_vccz .LD_tok32

.LD_join37:
	ds_read_b64 v[200:201], v249 offset:512
	ds_read_b64 v[202:203], v249 offset:2560
	ds_read_b64 v[204:205], v249 offset:4608
	ds_read_b64 v[206:207], v249 offset:6656
	s_waitcnt lgkmcnt(8)
	v_mfma_f32_32x32x16_f16 v[64:79], a[208:211], v[160:163], v[64:79]
	ds_read_b128 v[160:163], v193 offset:49152
	v_mfma_f32_32x32x16_f16 v[80:95], a[208:211], v[164:167], v[80:95]
	ds_read_b128 v[164:167], v193 offset:50176
	v_mfma_f32_32x32x16_f16 v[64:79], a[212:215], v[168:171], v[64:79]
	ds_read_b128 v[168:171], v193 offset:51200
	v_mfma_f32_32x32x16_f16 v[80:95], a[212:215], v[172:175], v[80:95]
	ds_read_b128 v[172:175], v193 offset:52224
	global_load_lds_dwordx4 v192, s[44:45] offset:3072 sc1
	s_waitcnt lgkmcnt(8)
	v_mfma_f32_32x32x16_f16 v[64:79], a[216:219], v[176:179], v[64:79]
	ds_read_b128 v[176:179], v193 offset:53248
	v_mfma_f32_32x32x16_f16 v[80:95], a[216:219], v[180:183], v[80:95]
	ds_read_b128 v[180:183], v193 offset:54272
	v_mfma_f32_32x32x16_f16 v[64:79], a[220:223], v[184:187], v[64:79]
	ds_read_b128 v[184:187], v193 offset:55296
	v_mfma_f32_32x32x16_f16 v[80:95], a[220:223], v[188:191], v[80:95]
	ds_read_b128 v[188:191], v193 offset:56320
	s_add_u32 s44, s34, 0x9000
	s_addc_u32 s45, s35, 0
	s_mov_b32 m0, s55
	s_nop 0
	global_load_lds_dwordx4 v192, s[44:45] sc1
	s_waitcnt lgkmcnt(4)
	v_mfma_f32_32x32x16_f16 v[64:79], a[224:227], v[160:163], v[64:79]
	ds_read_b128 v[160:163], v193 offset:57344
	v_mfma_f32_32x32x16_f16 v[80:95], a[224:227], v[164:167], v[80:95]
	ds_read_b128 v[164:167], v193 offset:58368
	v_mfma_f32_32x32x16_f16 v[64:79], a[228:231], v[168:171], v[64:79]
	ds_read_b128 v[168:171], v193 offset:59392
	v_mfma_f32_32x32x16_f16 v[80:95], a[228:231], v[172:175], v[80:95]
	ds_read_b128 v[172:175], v193 offset:60416
	global_load_lds_dwordx4 v192, s[44:45] offset:1024 sc1
	v_add_f32_e32 v200, v200, v202
	v_add_f32_e32 v201, v201, v203
	v_add_f32_e32 v200, v200, v204
	v_add_f32_e32 v201, v201, v205
	v_add_f32_e32 v200, v200, v206
	v_add_f32_e32 v201, v201, v207
	global_store_dwordx2 v250, v[200:201], s[72:73]
	s_waitcnt lgkmcnt(4)
	v_mfma_f32_32x32x16_f16 v[64:79], a[232:235], v[176:179], v[64:79]
	ds_read_b128 v[176:179], v193 offset:61440
	v_mfma_f32_32x32x16_f16 v[80:95], a[232:235], v[180:183], v[80:95]
	ds_read_b128 v[180:183], v193 offset:62464
	v_mfma_f32_32x32x16_f16 v[64:79], a[236:239], v[184:187], v[64:79]
	ds_read_b128 v[184:187], v193 offset:63488
	v_mfma_f32_32x32x16_f16 v[80:95], a[236:239], v[188:191], v[80:95]
	ds_read_b128 v[188:191], v193 offset:64512
	global_load_lds_dwordx4 v192, s[44:45] offset:2048 sc1
	s_and_b32 s64, s33, 1
	s_lshl_b32 s64, s64, 22
	s_add_u32 s64, s64, s50
	s_add_u32 s64, s64, 0x40000
	s_add_u32 s36, s6, s64
	s_addc_u32 s37, s7, 0
	s_lshl_b32 s64, s33, 3
	s_add_u32 s64, s64, s29
	s_lshl_b32 s64, s64, 5
	s_add_u32 s64, s64, s30
	s_lshl_b32 s64, s64, 2
	s_add_u32 s40, s8, s64
	s_addc_u32 s41, s9, 0
	s_lshl_b32 s64, s33, 19
	s_add_u32 s64, s64, 0x400
	s_add_u32 s72, s62, s64
	s_addc_u32 s73, s63, 0
	s_waitcnt vmcnt(9)
	s_barrier
	s_waitcnt lgkmcnt(4)
	v_mfma_f32_32x32x16_f16 v[64:79], a[240:243], v[160:163], v[64:79]
	ds_read_b128 v[160:163], v192 offset:0
	v_mfma_f32_32x32x16_f16 v[80:95], a[240:243], v[164:167], v[80:95]
	ds_read_b128 v[164:167], v192 offset:1024
	v_mfma_f32_32x32x16_f16 v[64:79], a[244:247], v[168:171], v[64:79]
	ds_read_b128 v[168:171], v192 offset:2048
	v_mfma_f32_32x32x16_f16 v[80:95], a[244:247], v[172:175], v[80:95]
	ds_read_b128 v[172:175], v192 offset:3072
	global_load_lds_dwordx4 v192, s[44:45] offset:3072 sc1
	s_waitcnt lgkmcnt(4)
	v_mfma_f32_32x32x16_f16 v[64:79], a[248:251], v[176:179], v[64:79]
	ds_read_b128 v[176:179], v192 offset:4096
	v_mfma_f32_32x32x16_f16 v[80:95], a[248:251], v[180:183], v[80:95]
	ds_read_b128 v[180:183], v192 offset:5120
	v_mfma_f32_32x32x16_f16 v[64:79], a[252:255], v[184:187], v[64:79]
	ds_read_b128 v[184:187], v192 offset:6144
	v_mfma_f32_32x32x16_f16 v[80:95], a[252:255], v[188:191], v[80:95]
	ds_read_b128 v[188:191], v192 offset:7168
	s_add_u32 s44, s34, 0x10000
	s_addc_u32 s45, s35, 0
	s_mov_b32 m0, s56
	s_nop 0
	global_load_lds_dwordx4 v192, s[44:45] sc1
	s_nop 3
	s_waitcnt lgkmcnt(4)
	v_mfma_f32_32x32x16_f16 v[96:111], a[0:3], v[160:163], v[96:111]
	ds_read_b128 v[160:163], v192 offset:8192
	v_exp_f32_e32 v200, v64
	v_mfma_f32_32x32x16_f16 v[112:127], a[0:3], v[164:167], v[112:127]
	ds_read_b128 v[164:167], v192 offset:9216
	s_lshl_b32 s64, s33, 3
	s_add_u32 s64, s64, s29
	s_lshl_b32 s64, s64, 7
	s_add_u32 s38, s8, s64
	s_addc_u32 s39, s9, 0
	global_load_dword v251, v196, s[38:39] sc1
	v_exp_f32_e32 v201, v65
	v_add_f32_e32 v200, 1.0, v200
	v_mfma_f32_32x32x16_f16 v[96:111], a[4:7], v[168:171], v[96:111]
	ds_read_b128 v[168:171], v192 offset:10240
	v_exp_f32_e32 v202, v66
	v_add_f32_e32 v201, 1.0, v201
	v_mfma_f32_32x32x16_f16 v[112:127], a[4:7], v[172:175], v[112:127]
	ds_read_b128 v[172:175], v192 offset:11264
	global_load_lds_dwordx4 v192, s[44:45] offset:1024 sc1
	v_exp_f32_e32 v203, v67
	v_add_f32_e32 v202, 1.0, v202
	s_waitcnt lgkmcnt(4)
	v_mfma_f32_32x32x16_f16 v[96:111], a[8:11], v[176:179], v[96:111]
	ds_read_b128 v[176:179], v192 offset:12288
	v_exp_f32_e32 v204, v68
	v_add_f32_e32 v203, 1.0, v203
	v_mfma_f32_32x32x16_f16 v[112:127], a[8:11], v[180:183], v[112:127]
	ds_read_b128 v[180:183], v192 offset:13312
	v_exp_f32_e32 v205, v69
	v_add_f32_e32 v204, 1.0, v204
	v_mfma_f32_32x32x16_f16 v[96:111], a[12:15], v[184:187], v[96:111]
	ds_read_b128 v[184:187], v192 offset:14336
	v_exp_f32_e32 v206, v70
	v_add_f32_e32 v205, 1.0, v205
	v_mfma_f32_32x32x16_f16 v[112:127], a[12:15], v[188:191], v[112:127]
	ds_read_b128 v[188:191], v192 offset:15360
	global_load_lds_dwordx4 v192, s[44:45] offset:2048 sc1
	v_exp_f32_e32 v207, v71
	v_add_f32_e32 v206, 1.0, v206
	s_waitcnt lgkmcnt(4)
	v_mfma_f32_32x32x16_f16 v[96:111], a[16:19], v[160:163], v[96:111]
	ds_read_b128 v[160:163], v192 offset:16384
	v_exp_f32_e32 v208, v72
	v_add_f32_e32 v207, 1.0, v207
	v_mfma_f32_32x32x16_f16 v[112:127], a[16:19], v[164:167], v[112:127]
	ds_read_b128 v[164:167], v192 offset:17408
	v_exp_f32_e32 v209, v73
	v_add_f32_e32 v208, 1.0, v208
	v_mfma_f32_32x32x16_f16 v[96:111], a[20:23], v[168:171], v[96:111]
	ds_read_b128 v[168:171], v192 offset:18432
	v_exp_f32_e32 v210, v74
	v_add_f32_e32 v209, 1.0, v209
	v_mfma_f32_32x32x16_f16 v[112:127], a[20:23], v[172:175], v[112:127]
	ds_read_b128 v[172:175], v192 offset:19456
	global_load_lds_dwordx4 v192, s[44:45] offset:3072 sc1
	v_exp_f32_e32 v211, v75
	v_add_f32_e32 v210, 1.0, v210
	s_waitcnt lgkmcnt(4)
	v_mfma_f32_32x32x16_f16 v[96:111], a[24:27], v[176:179], v[96:111]
	ds_read_b128 v[176:179], v192 offset:20480
	v_exp_f32_e32 v212, v76
	v_add_f32_e32 v211, 1.0, v211
	v_mfma_f32_32x32x16_f16 v[112:127], a[24:27], v[180:183], v[112:127]
	ds_read_b128 v[180:183], v192 offset:21504
	v_exp_f32_e32 v213, v77
	v_add_f32_e32 v212, 1.0, v212
	v_mfma_f32_32x32x16_f16 v[96:111], a[28:31], v[184:187], v[96:111]
	ds_read_b128 v[184:187], v192 offset:22528
	v_exp_f32_e32 v214, v78
	v_add_f32_e32 v213, 1.0, v213
	v_mfma_f32_32x32x16_f16 v[112:127], a[28:31], v[188:191], v[112:127]
	ds_read_b128 v[188:191], v192 offset:23552
	s_add_u32 s44, s34, 0x11000
	s_addc_u32 s45, s35, 0
	s_mov_b32 m0, s57
	s_nop 0
	global_load_lds_dwordx4 v192, s[44:45] sc1
	v_exp_f32_e32 v215, v79
	v_add_f32_e32 v214, 1.0, v214
	s_waitcnt lgkmcnt(4)
	v_mfma_f32_32x32x16_f16 v[96:111], a[32:35], v[160:163], v[96:111]
	ds_read_b128 v[160:163], v192 offset:24576
	v_add_f32_e32 v215, 1.0, v215
	v_rcp_f32_e32 v200, v200
	v_mfma_f32_32x32x16_f16 v[112:127], a[32:35], v[164:167], v[112:127]
	ds_read_b128 v[164:167], v192 offset:25600
	v_rcp_f32_e32 v201, v201
	v_mfma_f32_32x32x16_f16 v[96:111], a[36:39], v[168:171], v[96:111]
	ds_read_b128 v[168:171], v192 offset:26624
	v_rcp_f32_e32 v202, v202
	v_mfma_f32_32x32x16_f16 v[112:127], a[36:39], v[172:175], v[112:127]
	ds_read_b128 v[172:175], v192 offset:27648
	global_load_lds_dwordx4 v192, s[44:45] offset:1024 sc1
	v_rcp_f32_e32 v203, v203
	s_waitcnt lgkmcnt(4)
	v_mfma_f32_32x32x16_f16 v[96:111], a[40:43], v[176:179], v[96:111]
	ds_read_b128 v[176:179], v192 offset:28672
	v_rcp_f32_e32 v204, v204
	v_mfma_f32_32x32x16_f16 v[112:127], a[40:43], v[180:183], v[112:127]
	ds_read_b128 v[180:183], v192 offset:29696
	v_rcp_f32_e32 v205, v205
	v_mul_f32_e32 v204, v204, v144
	v_mfma_f32_32x32x16_f16 v[96:111], a[44:47], v[184:187], v[96:111]
	ds_read_b128 v[184:187], v192 offset:30720
	v_rcp_f32_e32 v206, v206
	v_mul_f32_e32 v205, v205, v145
	v_mfma_f32_32x32x16_f16 v[112:127], a[44:47], v[188:191], v[112:127]
	ds_read_b128 v[188:191], v192 offset:31744
	global_load_lds_dwordx4 v192, s[44:45] offset:2048 sc1
	v_rcp_f32_e32 v207, v207
	v_mul_f32_e32 v206, v206, v146
	s_waitcnt vmcnt(8)
	s_barrier
	s_waitcnt lgkmcnt(4)
	v_mfma_f32_32x32x16_f16 v[96:111], a[48:51], v[160:163], v[96:111]
	ds_read_b128 v[160:163], v192 offset:32768
	v_rcp_f32_e32 v208, v208
	v_mul_f32_e32 v207, v207, v147
	v_mfma_f32_32x32x16_f16 v[112:127], a[48:51], v[164:167], v[112:127]
	ds_read_b128 v[164:167], v192 offset:33792
	v_rcp_f32_e32 v209, v209
	v_fmamk_f32 v208, v208, 0xc0b8aa3b, v198
	v_mfma_f32_32x32x16_f16 v[96:111], a[52:55], v[168:171], v[96:111]
	ds_read_b128 v[168:171], v192 offset:34816
	v_rcp_f32_e32 v210, v210
	v_fmamk_f32 v209, v209, 0xc0b8aa3b, v198
	v_fma_f32 v144, v200, v208, v204
	v_mfma_f32_32x32x16_f16 v[112:127], a[52:55], v[172:175], v[112:127]
	ds_read_b128 v[172:175], v192 offset:35840
	global_load_lds_dwordx4 v192, s[44:45] offset:3072 sc1
	v_rcp_f32_e32 v211, v211
	v_fmamk_f32 v210, v210, 0xc0b8aa3b, v198
	v_fma_f32 v145, v201, v209, v205
	s_waitcnt lgkmcnt(4)
	v_mfma_f32_32x32x16_f16 v[96:111], a[56:59], v[176:179], v[96:111]
	ds_read_b128 v[176:179], v192 offset:36864
	v_rcp_f32_e32 v212, v212
	v_fmamk_f32 v211, v211, 0xc0b8aa3b, v198
	v_fma_f32 v146, v202, v210, v206
	v_mfma_f32_32x32x16_f16 v[112:127], a[56:59], v[180:183], v[112:127]
	ds_read_b128 v[180:183], v192 offset:37888
	v_rcp_f32_e32 v213, v213
	v_fma_f32 v147, v203, v211, v207
	v_mfma_f32_32x32x16_f16 v[96:111], a[60:63], v[184:187], v[96:111]
	ds_read_b128 v[184:187], v192 offset:38912
	v_rcp_f32_e32 v214, v214
	v_mfma_f32_32x32x16_f16 v[112:127], a[60:63], v[188:191], v[112:127]
	ds_read_b128 v[188:191], v192 offset:39936
	s_add_u32 s44, s34, 0x18000
	s_addc_u32 s45, s35, 0
	s_mov_b32 m0, s58
	s_nop 0
	global_load_lds_dwordx4 v192, s[44:45] sc1
	v_rcp_f32_e32 v215, v215
	s_waitcnt lgkmcnt(4)
	v_mfma_f32_32x32x16_f16 v[96:111], a[64:67], v[160:163], v[96:111]
	ds_read_b128 v[160:163], v192 offset:40960
	v_exp_f32_e32 v200, v144
	v_mfma_f32_32x32x16_f16 v[112:127], a[64:67], v[164:167], v[112:127]
	ds_read_b128 v[164:167], v192 offset:41984
	v_exp_f32_e32 v201, v145
	v_add_f32_e32 v200, 1.0, v200
	v_mfma_f32_32x32x16_f16 v[96:111], a[68:71], v[168:171], v[96:111]
	ds_read_b128 v[168:171], v192 offset:43008
	v_exp_f32_e32 v202, v146
	v_add_f32_e32 v201, 1.0, v201
	v_mfma_f32_32x32x16_f16 v[112:127], a[68:71], v[172:175], v[112:127]
	ds_read_b128 v[172:175], v192 offset:44032
	global_load_lds_dwordx4 v192, s[44:45] offset:1024 sc1
	v_exp_f32_e32 v203, v147
	v_add_f32_e32 v202, 1.0, v202
	s_waitcnt lgkmcnt(4)
	v_mfma_f32_32x32x16_f16 v[96:111], a[72:75], v[176:179], v[96:111]
	ds_read_b128 v[176:179], v192 offset:45056
	v_add_f32_e32 v203, 1.0, v203
	v_rcp_f32_e32 v200, v200
	v_mfma_f32_32x32x16_f16 v[112:127], a[72:75], v[180:183], v[112:127]
	ds_read_b128 v[180:183], v192 offset:46080
	v_rcp_f32_e32 v201, v201
	v_fma_f32 v200, v200, 2.0, -1.0
	v_mfma_f32_32x32x16_f16 v[96:111], a[76:79], v[184:187], v[96:111]
	ds_read_b128 v[184:187], v192 offset:47104
	v_rcp_f32_e32 v202, v202
	v_fma_f32 v201, v201, 2.0, -1.0
	v_mul_f32_e32 v216, v212, v200
	v_mfma_f32_32x32x16_f16 v[112:127], a[76:79], v[188:191], v[112:127]
	ds_read_b128 v[188:191], v192 offset:48128
	global_load_lds_dwordx4 v192, s[44:45] offset:2048 sc1
	v_rcp_f32_e32 v203, v203
	v_fma_f32 v202, v202, 2.0, -1.0
	v_mul_f32_e32 v217, v213, v201
	s_waitcnt lgkmcnt(4)
	v_mfma_f32_32x32x16_f16 v[96:111], a[80:83], v[160:163], v[96:111]
	ds_read_b128 v[160:163], v192 offset:49152
	v_fma_f32 v203, v203, 2.0, -1.0
	v_mul_f32_e32 v218, v214, v202
	v_exp_f32_e32 v200, v80
	v_mfma_f32_32x32x16_f16 v[112:127], a[80:83], v[164:167], v[112:127]
	ds_read_b128 v[164:167], v192 offset:50176
	v_mul_f32_e32 v219, v215, v203
	v_mul_f32_e32 v236, v216, v228
	v_exp_f32_e32 v201, v81
	v_mfma_f32_32x32x16_f16 v[96:111], a[84:87], v[168:171], v[96:111]
	ds_read_b128 v[168:171], v192 offset:51200
	v_mul_f32_e32 v237, v216, v232
	v_fmac_f32_e32 v236, v217, v229
	v_exp_f32_e32 v202, v82
	v_mfma_f32_32x32x16_f16 v[112:127], a[84:87], v[172:175], v[112:127]
	ds_read_b128 v[172:175], v192 offset:52224
	global_load_lds_dwordx4 v192, s[44:45] offset:3072 sc1
	v_fmac_f32_e32 v237, v217, v233
	v_fmac_f32_e32 v236, v218, v230
	v_exp_f32_e32 v203, v83
	s_waitcnt lgkmcnt(4)
	v_mfma_f32_32x32x16_f16 v[96:111], a[88:91], v[176:179], v[96:111]
	ds_read_b128 v[176:179], v192 offset:53248
	v_fmac_f32_e32 v237, v218, v234
	v_fmac_f32_e32 v236, v219, v231
	v_exp_f32_e32 v204, v84
	v_mfma_f32_32x32x16_f16 v[112:127], a[88:91], v[180:183], v[112:127]
	ds_read_b128 v[180:183], v192 offset:54272
	v_fmac_f32_e32 v237, v219, v235
	v_mov_b32_e32 v238, v236
	v_exp_f32_e32 v205, v85
	v_mfma_f32_32x32x16_f16 v[96:111], a[92:95], v[184:187], v[96:111]
	ds_read_b128 v[184:187], v192 offset:55296
	v_mov_b32_e32 v239, v236
	v_mov_b32_e32 v240, v237
	v_exp_f32_e32 v206, v86
	v_mfma_f32_32x32x16_f16 v[112:127], a[92:95], v[188:191], v[112:127]
	ds_read_b128 v[188:191], v192 offset:56320
	s_add_u32 s44, s34, 0x19000
	s_addc_u32 s45, s35, 0
	s_mov_b32 m0, s59
	s_nop 0
	global_load_lds_dwordx4 v192, s[44:45] sc1
	v_mov_b32_e32 v241, v237
	v_cvt_pk_f16_f32 v220, v216, v217
	v_exp_f32_e32 v207, v87
	s_waitcnt lgkmcnt(4)
	v_mfma_f32_32x32x16_f16 v[96:111], a[96:99], v[160:163], v[96:111]
	ds_read_b128 v[160:163], v192 offset:57344
	s_nop 1
	v_permlane32_swap_b32_e32 v238, v239
	v_permlane32_swap_b32_e32 v240, v241
	v_add_f32_e32 v238, v238, v239
	v_add_f32_e32 v239, v240, v241
	ds_write_b64 v248, v[238:239] offset:1024
	v_exp_f32_e32 v208, v88
	v_mfma_f32_32x32x16_f16 v[112:127], a[96:99], v[164:167], v[112:127]
	ds_read_b128 v[164:167], v192 offset:58368
	v_cvt_pk_f16_f32 v221, v218, v219
	v_exp_f32_e32 v209, v89
	v_add_f32_e32 v200, 1.0, v200
	v_mfma_f32_32x32x16_f16 v[96:111], a[100:103], v[168:171], v[96:111]
	ds_read_b128 v[168:171], v192 offset:59392
	v_exp_f32_e32 v210, v90
	v_add_f32_e32 v201, 1.0, v201
	v_add_f32_e32 v202, 1.0, v202
	v_mfma_f32_32x32x16_f16 v[112:127], a[100:103], v[172:175], v[112:127]
	ds_read_b128 v[172:175], v192 offset:60416
	global_load_lds_dwordx4 v192, s[44:45] offset:1024 sc1
	v_exp_f32_e32 v211, v91
	v_add_f32_e32 v203, 1.0, v203
	v_add_f32_e32 v204, 1.0, v204
	s_waitcnt lgkmcnt(5)
	v_mfma_f32_32x32x16_f16 v[96:111], a[104:107], v[176:179], v[96:111]
	ds_read_b128 v[176:179], v192 offset:61440
	v_exp_f32_e32 v212, v92
	v_add_f32_e32 v205, 1.0, v205
	v_add_f32_e32 v206, 1.0, v206
	v_mfma_f32_32x32x16_f16 v[112:127], a[104:107], v[180:183], v[112:127]
	ds_read_b128 v[180:183], v192 offset:62464
	v_exp_f32_e32 v213, v93
	v_add_f32_e32 v207, 1.0, v207
	v_add_f32_e32 v208, 1.0, v208
	v_mfma_f32_32x32x16_f16 v[96:111], a[108:111], v[184:187], v[96:111]
	ds_read_b128 v[184:187], v192 offset:63488
	v_exp_f32_e32 v214, v94
	v_add_f32_e32 v209, 1.0, v209
	v_add_f32_e32 v210, 1.0, v210
	v_mfma_f32_32x32x16_f16 v[112:127], a[108:111], v[188:191], v[112:127]
	ds_read_b128 v[188:191], v192 offset:64512
	global_load_lds_dwordx4 v192, s[44:45] offset:2048 sc1
	v_exp_f32_e32 v215, v95
	v_add_f32_e32 v211, 1.0, v211
	v_add_f32_e32 v212, 1.0, v212
	s_waitcnt vmcnt(7)
	s_barrier
	s_waitcnt lgkmcnt(4)
	v_mfma_f32_32x32x16_f16 v[96:111], a[112:115], v[160:163], v[96:111]
	ds_read_b128 v[160:163], v193 offset:0
	v_add_f32_e32 v213, 1.0, v213
	v_add_f32_e32 v214, 1.0, v214
	v_rcp_f32_e32 v200, v200
	v_mfma_f32_32x32x16_f16 v[112:127], a[112:115], v[164:167], v[112:127]
	ds_read_b128 v[164:167], v193 offset:1024
	v_add_f32_e32 v215, 1.0, v215
	v_rcp_f32_e32 v201, v201
	v_mfma_f32_32x32x16_f16 v[96:111], a[116:119], v[168:171], v[96:111]
	ds_read_b128 v[168:171], v193 offset:2048
	v_rcp_f32_e32 v202, v202
	v_mfma_f32_32x32x16_f16 v[112:127], a[116:119], v[172:175], v[112:127]
	ds_read_b128 v[172:175], v193 offset:3072
	global_load_lds_dwordx4 v192, s[44:45] offset:3072 sc1
	v_rcp_f32_e32 v203, v203
	s_waitcnt lgkmcnt(4)
	v_mfma_f32_32x32x16_f16 v[96:111], a[120:123], v[176:179], v[96:111]
	ds_read_b128 v[176:179], v193 offset:4096
	v_rcp_f32_e32 v204, v204
	s_add_u32 s46, s42, 0x2000
	s_addc_u32 s47, s43, 0
	global_load_dwordx4 v[32:35], v192, s[46:47] offset:0
	v_mfma_f32_32x32x16_f16 v[112:127], a[120:123], v[180:183], v[112:127]
	ds_read_b128 v[180:183], v193 offset:5120
	v_rcp_f32_e32 v205, v205
	v_mul_f32_e32 v204, v204, v148
	global_load_dwordx4 v[36:39], v192, s[46:47] offset:1024
	global_load_dwordx4 v[40:43], v192, s[46:47] offset:2048
	v_mfma_f32_32x32x16_f16 v[96:111], a[124:127], v[184:187], v[96:111]
	ds_read_b128 v[184:187], v193 offset:6144
	v_rcp_f32_e32 v206, v206
	v_mul_f32_e32 v205, v205, v149
	global_load_dwordx4 v[44:47], v192, s[46:47] offset:3072
	s_add_u32 s46, s42, 0x3000
	s_addc_u32 s47, s43, 0
	v_mfma_f32_32x32x16_f16 v[112:127], a[124:127], v[188:191], v[112:127]
	ds_read_b128 v[188:191], v193 offset:7168
	v_cmp_gt_u32_e32 vcc, 1, v251
	s_cbranch_vccz .LD_tok38
